# drop s_nop 15x3 pads behind the K-loops of P1/P8/P11/P18 and P11 header vmcnt(0) drain (on top of rope-in-LDS, G_P1=144)
# baseline (speedup 1.0000x reference)
; #define PG8_STAGE(bufoff, gbase, voff) do { _Pragma("unroll") for (int _i = 0; _i < 2; ++_i) \
;         __builtin_amdgcn_global_load_lds((const unsigned*)((const char*)(gbase) + (voff)[_i]), (PG8_LAS unsigned*)(lds + (bufoff) + ldsw + _i * 8192), 16, 0, 0); } while (0)
; #define PG8_STAGE_A(bufoff, gbase, h, nx) do { if constexpr (Sched::GATHER) { const unsigned vv_[2] = {(nx) ? vAn[h][0] : vA[h][0], (nx) ? vAn[h][1] : vA[h][1]}; PG8_STAGE(bufoff, gbase, vv_); } \
;         else { PG8_STAGE(bufoff, (gbase) + (h) * hstep, voffA); } } while (0)
; #define PG8_LDA(dst, b, h) do { _Pragma("unroll") for (int m = 0; m < 4; ++m) _Pragma("unroll") for (int k = 0; k < 2; ++k) dst[m][k] = *(const PG8_LAS bf16x8*)(lds + PG8_SA(b, h) + aoff + m * 2048 + k * 1024); } while (0)
; #define PG8_LDB(dst, b, h) do { _Pragma("unroll") for (int n = 0; n < 2; ++n) _Pragma("unroll") for (int k = 0; k < 2; ++k) dst[n][k] = *(const PG8_LAS bf16x8*)(lds + PG8_SB(b, h) + boff + n * 2048 + k * 1024); } while (0)
; #define PG8_WAIT_V(n) asm volatile("s_waitcnt vmcnt(" #n ")" ::: "memory")
; #define PG8_WAIT_L(n) asm volatile("s_waitcnt lgkmcnt(" #n ")" ::: "memory")
; #define PG8_BAR __builtin_amdgcn_s_barrier()
; #define PG8_SCHED __builtin_amdgcn_sched_barrier(0)
;     ...
;             PG8_LDB(B0, 0, 0); PG8_LDB(B1, 0, 1); PG8_SCHED; PG8_LDA(At, 0, 0); PG8_STAGE_A(PG8_SA(1, 1), a1, 1, false);
;             PG8_WAIT_V(8); PG8_WAIT_L(0); PG8_BAR; PG8_MMA(0, 0, At, B0); PG8_MMA(0, 1, At, B1); PG8_BAR; PG8_SCHED;
;             PG8_LDA(At, 0, 1); PG8_STAGE(PG8_SB(0, 0), b2, voffB); PG8_STAGE(PG8_SB(0, 1), b2 + hstepB, voffB); PG8_STAGE_A(PG8_SA(0, 0), a2, 0, last);
;             PG8_WAIT_V(8); PG8_WAIT_L(0); PG8_BAR; PG8_MMA(1, 0, At, B0); PG8_MMA(1, 1, At, B1); PG8_BAR; PG8_SCHED;
.LBB0_153:
	ds_read_b128 v[26:29], v205
	ds_read_b128 v[30:33], v205 offset:1024
	ds_read_b128 v[18:21], v205 offset:2048
	ds_read_b128 v[22:25], v205 offset:3072
	ds_read_b128 v[10:13], v206
	ds_read_b128 v[14:17], v206 offset:1024
	ds_read_b128 v[2:5], v206 offset:2048
	ds_read_b128 v[6:9], v206 offset:3072
	s_add_u32 s10, s8, 0xfffe0080
	s_addc_u32 s11, s9, -1
	s_cmp_eq_u32 s33, 4
	s_cselect_b32 s67, s0, s11
	s_cselect_b32 s66, s1, s10
	s_cselect_b32 s11, s5, s19
	s_cselect_b32 s10, s7, s18
	v_lshl_add_u64 v[162:163], s[8:9], 0, v[176:177]
	s_add_i32 m0, s82, 0xc000
	ds_read_b128 v[184:187], v207
	ds_read_b128 v[188:191], v207 offset:1024
	ds_read_b128 v[192:195], v207 offset:2048
	ds_read_b128 v[196:199], v207 offset:3072
	ds_read_b128 v[214:217], v207 offset:4096
	ds_read_b128 v[218:221], v207 offset:5120
	ds_read_b128 v[222:225], v207 offset:6144
	ds_read_b128 v[226:229], v207 offset:7168
	global_load_lds_dwordx4 v[162:163], off
	v_lshl_add_u64 v[162:163], s[8:9], 0, v[178:179]
	s_add_i32 m0, s82, 0xe000
	s_nop 0
	global_load_lds_dwordx4 v[162:163], off
	s_waitcnt vmcnt(8)
	s_waitcnt lgkmcnt(0)
	s_barrier
	s_setprio 1
	s_nop 3
	s_waitcnt lgkmcnt(0)
	v_mfma_scale_f32_16x16x128_f8f6f4 v[158:161], v[26:33], v[184:191], v[158:161], v208, v209 op_sel_hi:[0,0,0]
	v_mfma_scale_f32_16x16x128_f8f6f4 v[154:157], v[18:25], v[184:191], v[154:157], v208, v209 op_sel_hi:[0,0,0]
	v_mfma_scale_f32_16x16x128_f8f6f4 v[142:145], v[26:33], v[192:199], v[142:145], v208, v209 op_sel_hi:[0,0,0]
	v_mfma_scale_f32_16x16x128_f8f6f4 v[138:141], v[18:25], v[192:199], v[138:141], v208, v209 op_sel_hi:[0,0,0]
	v_mfma_scale_f32_16x16x128_f8f6f4 v[126:129], v[26:33], v[214:221], v[126:129], v208, v209 op_sel_hi:[0,0,0]
	v_mfma_scale_f32_16x16x128_f8f6f4 v[122:125], v[18:25], v[214:221], v[122:125], v208, v209 op_sel_hi:[0,0,0]
	v_mfma_scale_f32_16x16x128_f8f6f4 v[110:113], v[26:33], v[222:229], v[110:113], v208, v209 op_sel_hi:[0,0,0]
	v_mfma_scale_f32_16x16x128_f8f6f4 v[106:109], v[18:25], v[222:229], v[106:109], v208, v209 op_sel_hi:[0,0,0]
	s_setprio 0
	s_setprio 1
	s_nop 3
	v_mfma_scale_f32_16x16x128_f8f6f4 v[150:153], v[10:17], v[184:191], v[150:153], v208, v209 op_sel_hi:[0,0,0]
	v_mfma_scale_f32_16x16x128_f8f6f4 v[146:149], v[2:9], v[184:191], v[146:149], v208, v209 op_sel_hi:[0,0,0]
	v_mfma_scale_f32_16x16x128_f8f6f4 v[134:137], v[10:17], v[192:199], v[134:137], v208, v209 op_sel_hi:[0,0,0]
	v_mfma_scale_f32_16x16x128_f8f6f4 v[130:133], v[2:9], v[192:199], v[130:133], v208, v209 op_sel_hi:[0,0,0]
	v_mfma_scale_f32_16x16x128_f8f6f4 v[118:121], v[10:17], v[214:221], v[118:121], v208, v209 op_sel_hi:[0,0,0]
	v_mfma_scale_f32_16x16x128_f8f6f4 v[114:117], v[2:9], v[214:221], v[114:117], v208, v209 op_sel_hi:[0,0,0]
	v_mfma_scale_f32_16x16x128_f8f6f4 v[102:105], v[10:17], v[222:229], v[102:105], v208, v209 op_sel_hi:[0,0,0]
	v_mfma_scale_f32_16x16x128_f8f6f4 v[98:101], v[2:9], v[222:229], v[98:101], v208, v209 op_sel_hi:[0,0,0]
	s_setprio 0
	s_barrier
	s_add_i32 s59, s96, s77
	v_lshl_add_u64 v[162:163], s[10:11], 0, v[168:169]
	s_mov_b32 m0, s59
	ds_read_b128 v[188:191], v207 offset:16384
	ds_read_b128 v[192:195], v207 offset:17408
	ds_read_b128 v[214:217], v207 offset:18432
	ds_read_b128 v[218:221], v207 offset:19456
	ds_read_b128 v[222:225], v207 offset:20480
	ds_read_b128 v[226:229], v207 offset:21504
	ds_read_b128 v[230:233], v207 offset:22528
	ds_read_b128 v[234:237], v207 offset:23552
	global_load_lds_dwordx4 v[162:163], off
	s_add_i32 m0, s59, 0x2000
	s_add_u32 s68, s10, 0x8000
	v_lshl_add_u64 v[164:165], s[10:11], 0, v[172:173]
	s_addc_u32 s69, s11, 0
	s_add_i32 s59, s97, s77
	global_load_lds_dwordx4 v[164:165], off
	v_lshl_add_u64 v[184:185], s[68:69], 0, v[168:169]
	s_mov_b32 m0, s59
	v_lshl_add_u64 v[186:187], s[66:67], 0, v[170:171]
	global_load_lds_dwordx4 v[184:185], off
	v_lshl_add_u64 v[184:185], s[68:69], 0, v[172:173]
	s_add_i32 m0, s59, 0x2000
	s_nop 0
	global_load_lds_dwordx4 v[184:185], off
	v_lshl_add_u64 v[184:185], s[66:67], 0, v[166:167]
	s_mov_b32 m0, s82
	s_nop 0
	global_load_lds_dwordx4 v[184:185], off
	s_mov_b32 m0, s83
	s_nop 0
	global_load_lds_dwordx4 v[186:187], off
	s_waitcnt vmcnt(8)
	s_waitcnt lgkmcnt(0)
	s_barrier
	s_setprio 1
	s_nop 3
	s_waitcnt lgkmcnt(0)
	v_mfma_scale_f32_16x16x128_f8f6f4 v[94:97], v[26:33], v[188:195], v[94:97], v208, v209 op_sel_hi:[0,0,0]
	v_mfma_scale_f32_16x16x128_f8f6f4 v[90:93], v[18:25], v[188:195], v[90:93], v208, v209 op_sel_hi:[0,0,0]
	v_mfma_scale_f32_16x16x128_f8f6f4 v[78:81], v[26:33], v[214:221], v[78:81], v208, v209 op_sel_hi:[0,0,0]
	v_mfma_scale_f32_16x16x128_f8f6f4 v[74:77], v[18:25], v[214:221], v[74:77], v208, v209 op_sel_hi:[0,0,0]
	v_mfma_scale_f32_16x16x128_f8f6f4 v[62:65], v[26:33], v[222:229], v[62:65], v208, v209 op_sel_hi:[0,0,0]
	v_mfma_scale_f32_16x16x128_f8f6f4 v[58:61], v[18:25], v[222:229], v[58:61], v208, v209 op_sel_hi:[0,0,0]
	v_mfma_scale_f32_16x16x128_f8f6f4 v[46:49], v[26:33], v[230:237], v[46:49], v208, v209 op_sel_hi:[0,0,0]
	v_mfma_scale_f32_16x16x128_f8f6f4 v[42:45], v[18:25], v[230:237], v[42:45], v208, v209 op_sel_hi:[0,0,0]
	s_setprio 0
	s_setprio 1
	s_nop 3
	v_mfma_scale_f32_16x16x128_f8f6f4 v[86:89], v[10:17], v[188:195], v[86:89], v208, v209 op_sel_hi:[0,0,0]
	v_mfma_scale_f32_16x16x128_f8f6f4 v[82:85], v[2:9], v[188:195], v[82:85], v208, v209 op_sel_hi:[0,0,0]
	v_mfma_scale_f32_16x16x128_f8f6f4 v[70:73], v[10:17], v[214:221], v[70:73], v208, v209 op_sel_hi:[0,0,0]
	v_mfma_scale_f32_16x16x128_f8f6f4 v[66:69], v[2:9], v[214:221], v[66:69], v208, v209 op_sel_hi:[0,0,0]
	v_mfma_scale_f32_16x16x128_f8f6f4 v[54:57], v[10:17], v[222:229], v[54:57], v208, v209 op_sel_hi:[0,0,0]
	v_mfma_scale_f32_16x16x128_f8f6f4 v[50:53], v[2:9], v[222:229], v[50:53], v208, v209 op_sel_hi:[0,0,0]
	v_mfma_scale_f32_16x16x128_f8f6f4 v[38:41], v[10:17], v[230:237], v[38:41], v208, v209 op_sel_hi:[0,0,0]
	v_mfma_scale_f32_16x16x128_f8f6f4 v[34:37], v[2:9], v[230:237], v[34:37], v208, v209 op_sel_hi:[0,0,0]
	s_setprio 0
	s_barrier
; #define PG8_STAGE(bufoff, gbase, voff) do { _Pragma("unroll") for (int _i = 0; _i < 2; ++_i) \
;         __builtin_amdgcn_global_load_lds((const unsigned*)((const char*)(gbase) + (voff)[_i]), (PG8_LAS unsigned*)(lds + (bufoff) + ldsw + _i * 8192), 16, 0, 0); } while (0)
; #define PG8_STAGE_A(bufoff, gbase, h, nx) do { if constexpr (Sched::GATHER) { const unsigned vv_[2] = {(nx) ? vAn[h][0] : vA[h][0], (nx) ? vAn[h][1] : vA[h][1]}; PG8_STAGE(bufoff, gbase, vv_); } \
;         else { PG8_STAGE(bufoff, (gbase) + (h) * hstep, voffA); } } while (0)
; #define PG8_LDA(dst, b, h) do { _Pragma("unroll") for (int m = 0; m < 4; ++m) _Pragma("unroll") for (int k = 0; k < 2; ++k) dst[m][k] = *(const PG8_LAS bf16x8*)(lds + PG8_SA(b, h) + aoff + m * 2048 + k * 1024); } while (0)
; #define PG8_LDB(dst, b, h) do { _Pragma("unroll") for (int n = 0; n < 2; ++n) _Pragma("unroll") for (int k = 0; k < 2; ++k) dst[n][k] = *(const PG8_LAS bf16x8*)(lds + PG8_SB(b, h) + boff + n * 2048 + k * 1024); } while (0)
; #define PG8_WAIT_V(n) asm volatile("s_waitcnt vmcnt(" #n ")" ::: "memory")
; #define PG8_WAIT_L(n) asm volatile("s_waitcnt lgkmcnt(" #n ")" ::: "memory")
; #define PG8_BAR __builtin_amdgcn_s_barrier()
; #define PG8_SCHED __builtin_amdgcn_sched_barrier(0)
;     ...
;             PG8_LDB(B0, 1, 0); PG8_LDB(B1, 1, 1); PG8_SCHED; PG8_LDA(At, 1, 0); PG8_STAGE_A(PG8_SA(0, 1), a2, 1, last);
;             PG8_WAIT_V(8); PG8_WAIT_L(0); PG8_BAR; PG8_MMA(0, 0, At, B0); PG8_MMA(0, 1, At, B1); PG8_BAR; PG8_SCHED;
;             PG8_LDA(At, 1, 1); PG8_STAGE(PG8_SB(1, 0), b3, voffB); PG8_STAGE(PG8_SB(1, 1), b3 + hstepB, voffB); PG8_STAGE_A(PG8_SA(1, 0), a3, 0, last);
;             PG8_WAIT_V(8); PG8_WAIT_L(0); PG8_BAR; PG8_MMA(1, 0, At, B0); PG8_MMA(1, 1, At, B1); PG8_BAR; PG8_SCHED;
;     ...
;         if constexpr (F8) asm volatile("s_nop 15\n\ts_nop 15\n\ts_nop 15" ::: "memory");
	s_add_i32 s59, 0, 0x18000
	s_add_i32 s61, 0, 0x1c000
	v_add_u32_e32 v14, s59, v203
	v_add_u32_e32 v30, s61, v203
	ds_read_b128 v[2:5], v14
	ds_read_b128 v[6:9], v14 offset:1024
	ds_read_b128 v[10:13], v14 offset:2048
	ds_read_b128 v[14:17], v14 offset:3072
	ds_read_b128 v[18:21], v30
	ds_read_b128 v[22:25], v30 offset:1024
	ds_read_b128 v[26:29], v30 offset:2048
	ds_read_b128 v[30:33], v30 offset:3072
	s_add_u32 s66, s66, 0x20000
	s_addc_u32 s67, s67, 0
	s_mov_b32 m0, s84
	v_lshl_add_u64 v[196:197], s[66:67], 0, v[166:167]
	ds_read_b128 v[188:191], v207 offset:32768
	ds_read_b128 v[192:195], v207 offset:33792
	ds_read_b128 v[214:217], v207 offset:34816
	ds_read_b128 v[218:221], v207 offset:35840
	ds_read_b128 v[222:225], v207 offset:36864
	ds_read_b128 v[226:229], v207 offset:37888
	ds_read_b128 v[230:233], v207 offset:38912
	ds_read_b128 v[234:237], v207 offset:39936
	global_load_lds_dwordx4 v[196:197], off
	v_lshl_add_u64 v[196:197], s[66:67], 0, v[170:171]
	s_mov_b32 m0, s85
	s_nop 0
	global_load_lds_dwordx4 v[196:197], off
	s_waitcnt vmcnt(8)
	s_waitcnt lgkmcnt(0)
	s_barrier
	s_setprio 1
	s_nop 3
	s_waitcnt lgkmcnt(0)
	v_mfma_scale_f32_16x16x128_f8f6f4 v[158:161], v[2:9], v[188:195], v[158:161], v208, v209 op_sel_hi:[0,0,0]
	v_mfma_scale_f32_16x16x128_f8f6f4 v[154:157], v[10:17], v[188:195], v[154:157], v208, v209 op_sel_hi:[0,0,0]
	v_mfma_scale_f32_16x16x128_f8f6f4 v[142:145], v[2:9], v[214:221], v[142:145], v208, v209 op_sel_hi:[0,0,0]
	v_mfma_scale_f32_16x16x128_f8f6f4 v[138:141], v[10:17], v[214:221], v[138:141], v208, v209 op_sel_hi:[0,0,0]
	v_mfma_scale_f32_16x16x128_f8f6f4 v[126:129], v[2:9], v[222:229], v[126:129], v208, v209 op_sel_hi:[0,0,0]
	v_mfma_scale_f32_16x16x128_f8f6f4 v[122:125], v[10:17], v[222:229], v[122:125], v208, v209 op_sel_hi:[0,0,0]
	v_mfma_scale_f32_16x16x128_f8f6f4 v[110:113], v[2:9], v[230:237], v[110:113], v208, v209 op_sel_hi:[0,0,0]
	v_mfma_scale_f32_16x16x128_f8f6f4 v[106:109], v[10:17], v[230:237], v[106:109], v208, v209 op_sel_hi:[0,0,0]
	s_setprio 0
	s_setprio 1
	s_nop 3
	v_mfma_scale_f32_16x16x128_f8f6f4 v[150:153], v[18:25], v[188:195], v[150:153], v208, v209 op_sel_hi:[0,0,0]
	v_mfma_scale_f32_16x16x128_f8f6f4 v[146:149], v[26:33], v[188:195], v[146:149], v208, v209 op_sel_hi:[0,0,0]
	v_mfma_scale_f32_16x16x128_f8f6f4 v[134:137], v[18:25], v[214:221], v[134:137], v208, v209 op_sel_hi:[0,0,0]
	v_mfma_scale_f32_16x16x128_f8f6f4 v[130:133], v[26:33], v[214:221], v[130:133], v208, v209 op_sel_hi:[0,0,0]
	v_mfma_scale_f32_16x16x128_f8f6f4 v[118:121], v[18:25], v[222:229], v[118:121], v208, v209 op_sel_hi:[0,0,0]
	v_mfma_scale_f32_16x16x128_f8f6f4 v[114:117], v[26:33], v[222:229], v[114:117], v208, v209 op_sel_hi:[0,0,0]
	v_mfma_scale_f32_16x16x128_f8f6f4 v[102:105], v[18:25], v[230:237], v[102:105], v208, v209 op_sel_hi:[0,0,0]
	v_mfma_scale_f32_16x16x128_f8f6f4 v[98:101], v[26:33], v[230:237], v[98:101], v208, v209 op_sel_hi:[0,0,0]
	s_setprio 0
	s_barrier
	s_add_i32 s59, s59, s77
	v_lshl_add_u64 v[162:163], v[162:163], 0, s[40:41]
	s_mov_b32 m0, s59
	ds_read_b128 v[188:191], v207 offset:49152
	ds_read_b128 v[192:195], v207 offset:50176
	ds_read_b128 v[214:217], v207 offset:51200
	ds_read_b128 v[218:221], v207 offset:52224
	ds_read_b128 v[222:225], v207 offset:53248
	ds_read_b128 v[226:229], v207 offset:54272
	ds_read_b128 v[230:233], v207 offset:55296
	ds_read_b128 v[234:237], v207 offset:56320
	global_load_lds_dwordx4 v[162:163], off
	s_add_i32 m0, s59, 0x2000
	s_add_u32 s10, s10, 0x8080
	v_lshl_add_u64 v[162:163], v[164:165], 0, s[40:41]
	s_addc_u32 s11, s11, 0
	s_add_i32 s59, s61, s77
	global_load_lds_dwordx4 v[162:163], off
	v_lshl_add_u64 v[162:163], s[10:11], 0, v[168:169]
	s_mov_b32 m0, s59
	s_nop 0
	global_load_lds_dwordx4 v[162:163], off
	v_lshl_add_u64 v[162:163], s[10:11], 0, v[172:173]
	s_add_i32 m0, s59, 0x2000
	s_nop 0
	global_load_lds_dwordx4 v[162:163], off
	v_lshl_add_u64 v[162:163], v[184:185], 0, s[40:41]
	s_mov_b32 m0, s94
	s_nop 0
	global_load_lds_dwordx4 v[162:163], off
	v_lshl_add_u64 v[162:163], v[186:187], 0, s[40:41]
	s_mov_b32 m0, s95
	s_nop 0
	global_load_lds_dwordx4 v[162:163], off
	s_waitcnt vmcnt(8)
	s_waitcnt lgkmcnt(0)
	s_barrier
	s_setprio 1
	s_nop 3
	s_waitcnt lgkmcnt(0)
	v_mfma_scale_f32_16x16x128_f8f6f4 v[94:97], v[2:9], v[188:195], v[94:97], v208, v209 op_sel_hi:[0,0,0]
	v_mfma_scale_f32_16x16x128_f8f6f4 v[90:93], v[10:17], v[188:195], v[90:93], v208, v209 op_sel_hi:[0,0,0]
	v_mfma_scale_f32_16x16x128_f8f6f4 v[78:81], v[2:9], v[214:221], v[78:81], v208, v209 op_sel_hi:[0,0,0]
	v_mfma_scale_f32_16x16x128_f8f6f4 v[74:77], v[10:17], v[214:221], v[74:77], v208, v209 op_sel_hi:[0,0,0]
	v_mfma_scale_f32_16x16x128_f8f6f4 v[62:65], v[2:9], v[222:229], v[62:65], v208, v209 op_sel_hi:[0,0,0]
	v_mfma_scale_f32_16x16x128_f8f6f4 v[58:61], v[10:17], v[222:229], v[58:61], v208, v209 op_sel_hi:[0,0,0]
	v_mfma_scale_f32_16x16x128_f8f6f4 v[46:49], v[2:9], v[230:237], v[46:49], v208, v209 op_sel_hi:[0,0,0]
	v_mfma_scale_f32_16x16x128_f8f6f4 v[42:45], v[10:17], v[230:237], v[42:45], v208, v209 op_sel_hi:[0,0,0]
	s_setprio 0
	s_setprio 1
	s_nop 3
	v_mfma_scale_f32_16x16x128_f8f6f4 v[86:89], v[18:25], v[188:195], v[86:89], v208, v209 op_sel_hi:[0,0,0]
	v_mfma_scale_f32_16x16x128_f8f6f4 v[82:85], v[26:33], v[188:195], v[82:85], v208, v209 op_sel_hi:[0,0,0]
	v_mfma_scale_f32_16x16x128_f8f6f4 v[70:73], v[18:25], v[214:221], v[70:73], v208, v209 op_sel_hi:[0,0,0]
	v_mfma_scale_f32_16x16x128_f8f6f4 v[66:69], v[26:33], v[214:221], v[66:69], v208, v209 op_sel_hi:[0,0,0]
	v_mfma_scale_f32_16x16x128_f8f6f4 v[54:57], v[18:25], v[222:229], v[54:57], v208, v209 op_sel_hi:[0,0,0]
	v_mfma_scale_f32_16x16x128_f8f6f4 v[50:53], v[26:33], v[222:229], v[50:53], v208, v209 op_sel_hi:[0,0,0]
	v_mfma_scale_f32_16x16x128_f8f6f4 v[38:41], v[18:25], v[230:237], v[38:41], v208, v209 op_sel_hi:[0,0,0]
	v_mfma_scale_f32_16x16x128_f8f6f4 v[34:37], v[26:33], v[230:237], v[34:37], v208, v209 op_sel_hi:[0,0,0]
	s_setprio 0
	s_barrier
	s_add_i32 s33, s33, 2
	s_add_u32 s8, s8, 0x100
	s_addc_u32 s9, s9, 0
	s_add_u32 s18, s18, 0x100
	s_addc_u32 s19, s19, 0
	s_cmp_gt_u32 s33, 5
	s_cbranch_scc0 .LBB0_153
	s_and_b64 vcc, exec, s[42:43]
	s_cbranch_vccz .LBB0_156
	s_barrier

; #define PG8_STAGE(bufoff, gbase, voff) do { _Pragma("unroll") for (int _i = 0; _i < 2; ++_i) \
;         __builtin_amdgcn_global_load_lds((const unsigned*)((const char*)(gbase) + (voff)[_i]), (PG8_LAS unsigned*)(lds + (bufoff) + ldsw + _i * 8192), 16, 0, 0); } while (0)
; #define PG8_STAGE_A(bufoff, gbase, h, nx) do { if constexpr (Sched::GATHER) { const unsigned vv_[2] = {(nx) ? vAn[h][0] : vA[h][0], (nx) ? vAn[h][1] : vA[h][1]}; PG8_STAGE(bufoff, gbase, vv_); } \
;         else { PG8_STAGE(bufoff, (gbase) + (h) * hstep, voffA); } } while (0)
; #define PG8_LDA(dst, b, h) do { _Pragma("unroll") for (int m = 0; m < 4; ++m) _Pragma("unroll") for (int k = 0; k < 2; ++k) dst[m][k] = *(const PG8_LAS bf16x8*)(lds + PG8_SA(b, h) + aoff + m * 2048 + k * 1024); } while (0)
; #define PG8_LDB(dst, b, h) do { _Pragma("unroll") for (int n = 0; n < 2; ++n) _Pragma("unroll") for (int k = 0; k < 2; ++k) dst[n][k] = *(const PG8_LAS bf16x8*)(lds + PG8_SB(b, h) + boff + n * 2048 + k * 1024); } while (0)
; #define PG8_WAIT_V(n) asm volatile("s_waitcnt vmcnt(" #n ")" ::: "memory")
; #define PG8_WAIT_L(n) asm volatile("s_waitcnt lgkmcnt(" #n ")" ::: "memory")
; #define PG8_BAR __builtin_amdgcn_s_barrier()
; #define PG8_SCHED __builtin_amdgcn_sched_barrier(0)
;     ...
;             PG8_LDB(B0, 0, 0); PG8_LDB(B1, 0, 1); PG8_SCHED; PG8_LDA(At, 0, 0); PG8_STAGE_A(PG8_SA(1, 1), a1, 1, false);
;             PG8_WAIT_V(8); PG8_WAIT_L(0); PG8_BAR; PG8_MMA(0, 0, At, B0); PG8_MMA(0, 1, At, B1); PG8_BAR; PG8_SCHED;
;             PG8_LDA(At, 0, 1); PG8_STAGE(PG8_SB(0, 0), b2, voffB); PG8_STAGE(PG8_SB(0, 1), b2 + hstepB, voffB); PG8_STAGE_A(PG8_SA(0, 0), a2, 0, last);
;             PG8_WAIT_V(8); PG8_WAIT_L(0); PG8_BAR; PG8_MMA(1, 0, At, B0); PG8_MMA(1, 1, At, B1); PG8_BAR; PG8_SCHED;
.LBB0_841:
	ds_read_b128 v[26:29], v194
	ds_read_b128 v[30:33], v194 offset:1024
	ds_read_b128 v[18:21], v194 offset:2048
	ds_read_b128 v[22:25], v194 offset:3072
	ds_read_b128 v[10:13], v195
	ds_read_b128 v[14:17], v195 offset:1024
	ds_read_b128 v[2:5], v195 offset:2048
	ds_read_b128 v[6:9], v195 offset:3072
	s_add_u32 s20, s54, s4
	s_addc_u32 s21, s55, s5
	s_add_u32 s22, s20, 0x25400100
	s_addc_u32 s23, s21, 0
	s_add_u32 s52, s49, s4
	s_addc_u32 s53, s50, s5
	s_cmpk_eq_i32 s4, 0x300
	s_cselect_b64 vcc, -1, 0
	s_and_b64 s[20:21], vcc, exec
	s_cselect_b32 s23, s93, s23
	s_cselect_b32 s22, s92, s22
	s_cselect_b32 s21, s17, s53
	s_cselect_b32 s20, s48, s52
	s_mov_b32 m0, s36
	v_lshl_add_u64 v[232:233], v[180:181], 0, s[4:5]
	ds_read_b128 v[182:185], v196
	ds_read_b128 v[186:189], v196 offset:1024
	ds_read_b128 v[208:211], v196 offset:2048
	ds_read_b128 v[212:215], v196 offset:3072
	ds_read_b128 v[216:219], v196 offset:4096
	ds_read_b128 v[220:223], v196 offset:5120
	ds_read_b128 v[224:227], v196 offset:6144
	ds_read_b128 v[228:231], v196 offset:7168
	global_load_lds_dwordx4 v[232:233], off
	v_lshl_add_u64 v[232:233], v[178:179], 0, s[4:5]
	s_mov_b32 m0, s37
	s_nop 0
	global_load_lds_dwordx4 v[232:233], off
	s_waitcnt vmcnt(8)
	s_waitcnt lgkmcnt(0)
	s_barrier
	s_setprio 1
	s_nop 3
	s_waitcnt lgkmcnt(0)
	v_mfma_scale_f32_16x16x128_f8f6f4 v[158:161], v[26:33], v[182:189], v[158:161], v197, v198 op_sel_hi:[0,0,0]
	v_mfma_scale_f32_16x16x128_f8f6f4 v[150:153], v[18:25], v[182:189], v[150:153], v197, v198 op_sel_hi:[0,0,0]
	v_mfma_scale_f32_16x16x128_f8f6f4 v[142:145], v[26:33], v[208:215], v[142:145], v197, v198 op_sel_hi:[0,0,0]
	v_mfma_scale_f32_16x16x128_f8f6f4 v[134:137], v[18:25], v[208:215], v[134:137], v197, v198 op_sel_hi:[0,0,0]
	v_mfma_scale_f32_16x16x128_f8f6f4 v[126:129], v[26:33], v[216:223], v[126:129], v197, v198 op_sel_hi:[0,0,0]
	v_mfma_scale_f32_16x16x128_f8f6f4 v[118:121], v[18:25], v[216:223], v[118:121], v197, v198 op_sel_hi:[0,0,0]
	v_mfma_scale_f32_16x16x128_f8f6f4 v[110:113], v[26:33], v[224:231], v[110:113], v197, v198 op_sel_hi:[0,0,0]
	v_mfma_scale_f32_16x16x128_f8f6f4 v[98:101], v[18:25], v[224:231], v[98:101], v197, v198 op_sel_hi:[0,0,0]
	s_setprio 0
	s_setprio 1
	s_nop 3
	v_mfma_scale_f32_16x16x128_f8f6f4 v[154:157], v[10:17], v[182:189], v[154:157], v197, v198 op_sel_hi:[0,0,0]
	v_mfma_scale_f32_16x16x128_f8f6f4 v[146:149], v[2:9], v[182:189], v[146:149], v197, v198 op_sel_hi:[0,0,0]
	v_mfma_scale_f32_16x16x128_f8f6f4 v[138:141], v[10:17], v[208:215], v[138:141], v197, v198 op_sel_hi:[0,0,0]
	v_mfma_scale_f32_16x16x128_f8f6f4 v[130:133], v[2:9], v[208:215], v[130:133], v197, v198 op_sel_hi:[0,0,0]
	v_mfma_scale_f32_16x16x128_f8f6f4 v[122:125], v[10:17], v[216:223], v[122:125], v197, v198 op_sel_hi:[0,0,0]
	v_mfma_scale_f32_16x16x128_f8f6f4 v[114:117], v[2:9], v[216:223], v[114:117], v197, v198 op_sel_hi:[0,0,0]
	v_mfma_scale_f32_16x16x128_f8f6f4 v[106:109], v[10:17], v[224:231], v[106:109], v197, v198 op_sel_hi:[0,0,0]
	v_mfma_scale_f32_16x16x128_f8f6f4 v[94:97], v[2:9], v[224:231], v[94:97], v197, v198 op_sel_hi:[0,0,0]
	s_setprio 0
	s_barrier
	s_mov_b32 m0, s38
	v_lshl_add_u64 v[182:183], s[20:21], 0, v[164:165]
	s_add_u32 s52, s20, 0x20000
	ds_read_b128 v[208:211], v196 offset:16384
	ds_read_b128 v[212:215], v196 offset:17408
	ds_read_b128 v[216:219], v196 offset:18432
	ds_read_b128 v[220:223], v196 offset:19456
	ds_read_b128 v[224:227], v196 offset:20480
	ds_read_b128 v[228:231], v196 offset:21504
	ds_read_b128 v[232:235], v196 offset:22528
	ds_read_b128 v[236:239], v196 offset:23552
	global_load_lds_dwordx4 v[182:183], off
	v_lshl_add_u64 v[184:185], s[20:21], 0, v[162:163]
	s_mov_b32 m0, s39
	s_addc_u32 s53, s21, 0
	global_load_lds_dwordx4 v[184:185], off
	v_lshl_add_u64 v[186:187], s[52:53], 0, v[164:165]
	s_mov_b32 m0, s40
	v_cndmask_b32_e32 v166, v206, v202, vcc
	global_load_lds_dwordx4 v[186:187], off
	v_lshl_add_u64 v[186:187], s[52:53], 0, v[162:163]
	s_mov_b32 m0, s41
	v_lshl_add_u64 v[188:189], s[22:23], 0, v[166:167]
	global_load_lds_dwordx4 v[186:187], off
	s_mov_b32 m0, s26
	v_cndmask_b32_e32 v186, v172, v203, vcc
	global_load_lds_dwordx4 v166, s[22:23]
	s_mov_b32 m0, s27
	v_mov_b32_e32 v187, v167
	global_load_lds_dwordx4 v186, s[22:23]
	s_waitcnt vmcnt(8)
	s_waitcnt lgkmcnt(0)
	v_lshl_add_u64 v[186:187], s[22:23], 0, v[186:187]
	s_barrier
	s_setprio 1
	s_nop 3
	s_waitcnt lgkmcnt(0)
	v_mfma_scale_f32_16x16x128_f8f6f4 v[82:85], v[26:33], v[208:215], v[82:85], v197, v198 op_sel_hi:[0,0,0]
	v_mfma_scale_f32_16x16x128_f8f6f4 v[70:73], v[18:25], v[208:215], v[70:73], v197, v198 op_sel_hi:[0,0,0]
	v_mfma_scale_f32_16x16x128_f8f6f4 v[78:81], v[26:33], v[216:223], v[78:81], v197, v198 op_sel_hi:[0,0,0]
	v_mfma_scale_f32_16x16x128_f8f6f4 v[66:69], v[18:25], v[216:223], v[66:69], v197, v198 op_sel_hi:[0,0,0]
	v_mfma_scale_f32_16x16x128_f8f6f4 v[58:61], v[26:33], v[224:231], v[58:61], v197, v198 op_sel_hi:[0,0,0]
	v_mfma_scale_f32_16x16x128_f8f6f4 v[50:53], v[18:25], v[224:231], v[50:53], v197, v198 op_sel_hi:[0,0,0]
	v_mfma_scale_f32_16x16x128_f8f6f4 v[42:45], v[26:33], v[232:239], v[42:45], v197, v198 op_sel_hi:[0,0,0]
	v_mfma_scale_f32_16x16x128_f8f6f4 v[34:37], v[18:25], v[232:239], v[34:37], v197, v198 op_sel_hi:[0,0,0]
	s_setprio 0
	s_setprio 1
	s_nop 3
	v_mfma_scale_f32_16x16x128_f8f6f4 v[102:105], v[10:17], v[208:215], v[102:105], v197, v198 op_sel_hi:[0,0,0]
	v_mfma_scale_f32_16x16x128_f8f6f4 v[90:93], v[2:9], v[208:215], v[90:93], v197, v198 op_sel_hi:[0,0,0]
	v_mfma_scale_f32_16x16x128_f8f6f4 v[86:89], v[10:17], v[216:223], v[86:89], v197, v198 op_sel_hi:[0,0,0]
	v_mfma_scale_f32_16x16x128_f8f6f4 v[74:77], v[2:9], v[216:223], v[74:77], v197, v198 op_sel_hi:[0,0,0]
	v_mfma_scale_f32_16x16x128_f8f6f4 v[62:65], v[10:17], v[224:231], v[62:65], v197, v198 op_sel_hi:[0,0,0]
	v_mfma_scale_f32_16x16x128_f8f6f4 v[54:57], v[2:9], v[224:231], v[54:57], v197, v198 op_sel_hi:[0,0,0]
	v_mfma_scale_f32_16x16x128_f8f6f4 v[46:49], v[10:17], v[232:239], v[46:49], v197, v198 op_sel_hi:[0,0,0]
	v_mfma_scale_f32_16x16x128_f8f6f4 v[38:41], v[2:9], v[232:239], v[38:41], v197, v198 op_sel_hi:[0,0,0]
	s_setprio 0
	s_barrier
; #define PG8_STAGE(bufoff, gbase, voff) do { _Pragma("unroll") for (int _i = 0; _i < 2; ++_i) \
;         __builtin_amdgcn_global_load_lds((const unsigned*)((const char*)(gbase) + (voff)[_i]), (PG8_LAS unsigned*)(lds + (bufoff) + ldsw + _i * 8192), 16, 0, 0); } while (0)
; #define PG8_STAGE_A(bufoff, gbase, h, nx) do { if constexpr (Sched::GATHER) { const unsigned vv_[2] = {(nx) ? vAn[h][0] : vA[h][0], (nx) ? vAn[h][1] : vA[h][1]}; PG8_STAGE(bufoff, gbase, vv_); } \
;         else { PG8_STAGE(bufoff, (gbase) + (h) * hstep, voffA); } } while (0)
; #define PG8_LDA(dst, b, h) do { _Pragma("unroll") for (int m = 0; m < 4; ++m) _Pragma("unroll") for (int k = 0; k < 2; ++k) dst[m][k] = *(const PG8_LAS bf16x8*)(lds + PG8_SA(b, h) + aoff + m * 2048 + k * 1024); } while (0)
; #define PG8_LDB(dst, b, h) do { _Pragma("unroll") for (int n = 0; n < 2; ++n) _Pragma("unroll") for (int k = 0; k < 2; ++k) dst[n][k] = *(const PG8_LAS bf16x8*)(lds + PG8_SB(b, h) + boff + n * 2048 + k * 1024); } while (0)
; #define PG8_WAIT_V(n) asm volatile("s_waitcnt vmcnt(" #n ")" ::: "memory")
; #define PG8_WAIT_L(n) asm volatile("s_waitcnt lgkmcnt(" #n ")" ::: "memory")
; #define PG8_BAR __builtin_amdgcn_s_barrier()
; #define PG8_SCHED __builtin_amdgcn_sched_barrier(0)
;     ...
;             PG8_LDB(B0, 1, 0); PG8_LDB(B1, 1, 1); PG8_SCHED; PG8_LDA(At, 1, 0); PG8_STAGE_A(PG8_SA(0, 1), a2, 1, last);
;             PG8_WAIT_V(8); PG8_WAIT_L(0); PG8_BAR; PG8_MMA(0, 0, At, B0); PG8_MMA(0, 1, At, B1); PG8_BAR; PG8_SCHED;
;             PG8_LDA(At, 1, 1); PG8_STAGE(PG8_SB(1, 0), b3, voffB); PG8_STAGE(PG8_SB(1, 1), b3 + hstepB, voffB); PG8_STAGE_A(PG8_SA(1, 0), a3, 0, last);
;             PG8_WAIT_V(8); PG8_WAIT_L(0); PG8_BAR; PG8_MMA(1, 0, At, B0); PG8_MMA(1, 1, At, B1); PG8_BAR; PG8_SCHED;
;     ...
;         if constexpr (F8) asm volatile("s_nop 15\n\ts_nop 15\n\ts_nop 15" ::: "memory");
	ds_read_b128 v[2:5], v199
	ds_read_b128 v[6:9], v199 offset:1024
	ds_read_b128 v[10:13], v199 offset:2048
	ds_read_b128 v[14:17], v199 offset:3072
	ds_read_b128 v[18:21], v200
	ds_read_b128 v[22:25], v200 offset:1024
	ds_read_b128 v[26:29], v200 offset:2048
	ds_read_b128 v[30:33], v200 offset:3072
	s_mov_b32 m0, s28
	v_cndmask_b32_e32 v166, v174, v204, vcc
	ds_read_b128 v[208:211], v196 offset:32768
	ds_read_b128 v[212:215], v196 offset:33792
	ds_read_b128 v[216:219], v196 offset:34816
	ds_read_b128 v[220:223], v196 offset:35840
	ds_read_b128 v[224:227], v196 offset:36864
	ds_read_b128 v[228:231], v196 offset:37888
	ds_read_b128 v[232:235], v196 offset:38912
	ds_read_b128 v[236:239], v196 offset:39936
	v_cndmask_b32_e32 v175, v176, v205, vcc
	global_load_lds_dwordx4 v166, s[22:23]
	s_mov_b32 m0, s29
	s_nop 0
	global_load_lds_dwordx4 v175, s[22:23]
	s_waitcnt vmcnt(8)
	s_waitcnt lgkmcnt(0)
	s_barrier
	s_setprio 1
	s_nop 3
	s_waitcnt lgkmcnt(0)
	v_mfma_scale_f32_16x16x128_f8f6f4 v[158:161], v[2:9], v[208:215], v[158:161], v197, v198 op_sel_hi:[0,0,0]
	v_mfma_scale_f32_16x16x128_f8f6f4 v[150:153], v[10:17], v[208:215], v[150:153], v197, v198 op_sel_hi:[0,0,0]
	v_mfma_scale_f32_16x16x128_f8f6f4 v[142:145], v[2:9], v[216:223], v[142:145], v197, v198 op_sel_hi:[0,0,0]
	v_mfma_scale_f32_16x16x128_f8f6f4 v[134:137], v[10:17], v[216:223], v[134:137], v197, v198 op_sel_hi:[0,0,0]
	v_mfma_scale_f32_16x16x128_f8f6f4 v[126:129], v[2:9], v[224:231], v[126:129], v197, v198 op_sel_hi:[0,0,0]
	v_mfma_scale_f32_16x16x128_f8f6f4 v[118:121], v[10:17], v[224:231], v[118:121], v197, v198 op_sel_hi:[0,0,0]
	v_mfma_scale_f32_16x16x128_f8f6f4 v[110:113], v[2:9], v[232:239], v[110:113], v197, v198 op_sel_hi:[0,0,0]
	v_mfma_scale_f32_16x16x128_f8f6f4 v[98:101], v[10:17], v[232:239], v[98:101], v197, v198 op_sel_hi:[0,0,0]
	s_setprio 0
	s_setprio 1
	s_nop 3
	v_mfma_scale_f32_16x16x128_f8f6f4 v[154:157], v[18:25], v[208:215], v[154:157], v197, v198 op_sel_hi:[0,0,0]
	v_mfma_scale_f32_16x16x128_f8f6f4 v[146:149], v[26:33], v[208:215], v[146:149], v197, v198 op_sel_hi:[0,0,0]
	v_mfma_scale_f32_16x16x128_f8f6f4 v[138:141], v[18:25], v[216:223], v[138:141], v197, v198 op_sel_hi:[0,0,0]
	v_mfma_scale_f32_16x16x128_f8f6f4 v[130:133], v[26:33], v[216:223], v[130:133], v197, v198 op_sel_hi:[0,0,0]
	v_mfma_scale_f32_16x16x128_f8f6f4 v[122:125], v[18:25], v[224:231], v[122:125], v197, v198 op_sel_hi:[0,0,0]
	v_mfma_scale_f32_16x16x128_f8f6f4 v[114:117], v[26:33], v[224:231], v[114:117], v197, v198 op_sel_hi:[0,0,0]
	v_mfma_scale_f32_16x16x128_f8f6f4 v[106:109], v[18:25], v[232:239], v[106:109], v197, v198 op_sel_hi:[0,0,0]
	v_mfma_scale_f32_16x16x128_f8f6f4 v[94:97], v[26:33], v[232:239], v[94:97], v197, v198 op_sel_hi:[0,0,0]
	s_setprio 0
	s_barrier
	s_mov_b32 m0, s42
	v_lshl_add_u64 v[182:183], v[182:183], 0, s[10:11]
	s_add_u32 s20, s20, 0x20080
	ds_read_b128 v[208:211], v196 offset:49152
	ds_read_b128 v[212:215], v196 offset:50176
	ds_read_b128 v[216:219], v196 offset:51200
	ds_read_b128 v[220:223], v196 offset:52224
	ds_read_b128 v[224:227], v196 offset:53248
	ds_read_b128 v[228:231], v196 offset:54272
	ds_read_b128 v[232:235], v196 offset:55296
	ds_read_b128 v[236:239], v196 offset:56320
	global_load_lds_dwordx4 v[182:183], off
	v_lshl_add_u64 v[182:183], v[184:185], 0, s[10:11]
	s_mov_b32 m0, s43
	s_addc_u32 s21, s21, 0
	global_load_lds_dwordx4 v[182:183], off
	v_lshl_add_u64 v[182:183], s[20:21], 0, v[164:165]
	s_mov_b32 m0, s44
	s_nop 0
	global_load_lds_dwordx4 v[182:183], off
	v_lshl_add_u64 v[182:183], s[20:21], 0, v[162:163]
	s_add_i32 m0, s44, 0x2000
	s_nop 0
	global_load_lds_dwordx4 v[182:183], off
	v_lshl_add_u64 v[182:183], v[188:189], 0, s[10:11]
	s_mov_b32 m0, s31
	s_nop 0
	global_load_lds_dwordx4 v[182:183], off
	v_lshl_add_u64 v[182:183], v[186:187], 0, s[10:11]
	s_mov_b32 m0, s34
	s_nop 0
	global_load_lds_dwordx4 v[182:183], off
	s_waitcnt vmcnt(8)
	s_waitcnt lgkmcnt(0)
	s_barrier
	s_setprio 1
	s_nop 3
	s_waitcnt lgkmcnt(0)
	v_mfma_scale_f32_16x16x128_f8f6f4 v[82:85], v[2:9], v[208:215], v[82:85], v197, v198 op_sel_hi:[0,0,0]
	v_mfma_scale_f32_16x16x128_f8f6f4 v[70:73], v[10:17], v[208:215], v[70:73], v197, v198 op_sel_hi:[0,0,0]
	v_mfma_scale_f32_16x16x128_f8f6f4 v[78:81], v[2:9], v[216:223], v[78:81], v197, v198 op_sel_hi:[0,0,0]
	v_mfma_scale_f32_16x16x128_f8f6f4 v[66:69], v[10:17], v[216:223], v[66:69], v197, v198 op_sel_hi:[0,0,0]
	v_mfma_scale_f32_16x16x128_f8f6f4 v[58:61], v[2:9], v[224:231], v[58:61], v197, v198 op_sel_hi:[0,0,0]
	v_mfma_scale_f32_16x16x128_f8f6f4 v[50:53], v[10:17], v[224:231], v[50:53], v197, v198 op_sel_hi:[0,0,0]
	v_mfma_scale_f32_16x16x128_f8f6f4 v[42:45], v[2:9], v[232:239], v[42:45], v197, v198 op_sel_hi:[0,0,0]
	v_mfma_scale_f32_16x16x128_f8f6f4 v[34:37], v[10:17], v[232:239], v[34:37], v197, v198 op_sel_hi:[0,0,0]
	s_setprio 0
	s_setprio 1
	s_nop 3
	v_mfma_scale_f32_16x16x128_f8f6f4 v[102:105], v[18:25], v[208:215], v[102:105], v197, v198 op_sel_hi:[0,0,0]
	v_mfma_scale_f32_16x16x128_f8f6f4 v[90:93], v[26:33], v[208:215], v[90:93], v197, v198 op_sel_hi:[0,0,0]
	v_mfma_scale_f32_16x16x128_f8f6f4 v[86:89], v[18:25], v[216:223], v[86:89], v197, v198 op_sel_hi:[0,0,0]
	v_mfma_scale_f32_16x16x128_f8f6f4 v[74:77], v[26:33], v[216:223], v[74:77], v197, v198 op_sel_hi:[0,0,0]
	v_mfma_scale_f32_16x16x128_f8f6f4 v[62:65], v[18:25], v[224:231], v[62:65], v197, v198 op_sel_hi:[0,0,0]
	v_mfma_scale_f32_16x16x128_f8f6f4 v[54:57], v[26:33], v[224:231], v[54:57], v197, v198 op_sel_hi:[0,0,0]
	v_mfma_scale_f32_16x16x128_f8f6f4 v[46:49], v[18:25], v[232:239], v[46:49], v197, v198 op_sel_hi:[0,0,0]
	v_mfma_scale_f32_16x16x128_f8f6f4 v[38:41], v[26:33], v[232:239], v[38:41], v197, v198 op_sel_hi:[0,0,0]
	s_setprio 0
	s_barrier
	s_add_i32 s51, s51, 2
	s_add_u32 s4, s4, 0x100
	s_addc_u32 s5, s5, 0
	s_cmp_gt_u32 s51, 5
	s_cbranch_scc0 .LBB0_841
	s_and_b64 vcc, exec, s[14:15]
	s_cbranch_vccz .LBB0_844
	s_barrier

; #define PG8_STAGE(bufoff, gbase, voff) do { _Pragma("unroll") for (int _i = 0; _i < 2; ++_i) \
;         __builtin_amdgcn_global_load_lds((const unsigned*)((const char*)(gbase) + (voff)[_i]), (PG8_LAS unsigned*)(lds + (bufoff) + ldsw + _i * 8192), 16, 0, 0); } while (0)
; #define PG8_STAGE_A(bufoff, gbase, h, nx) do { if constexpr (Sched::GATHER) { const unsigned vv_[2] = {(nx) ? vAn[h][0] : vA[h][0], (nx) ? vAn[h][1] : vA[h][1]}; PG8_STAGE(bufoff, gbase, vv_); } \
;         else { PG8_STAGE(bufoff, (gbase) + (h) * hstep, voffA); } } while (0)
; #define PG8_LDA(dst, b, h) do { _Pragma("unroll") for (int m = 0; m < 4; ++m) _Pragma("unroll") for (int k = 0; k < 2; ++k) dst[m][k] = *(const PG8_LAS bf16x8*)(lds + PG8_SA(b, h) + aoff + m * 2048 + k * 1024); } while (0)
; #define PG8_WAIT_V(n) asm volatile("s_waitcnt vmcnt(" #n ")" ::: "memory")
; #define PG8_WAIT_L(n) asm volatile("s_waitcnt lgkmcnt(" #n ")" ::: "memory")
;     ...
;         const bool has_next = S.next(ui + 1, nxt);
;         const char* nA = Sched::GATHER ? cA : (has_next ? (const char*)g.A + (size_t)nxt.pm * tstep : cA);
;         if constexpr (Sched::GATHER) { if (has_next) { PG8_AOFF(vAn, ui + 1); } else { _Pragma("unroll") for (int h_ = 0; h_ < 2; ++h_) _Pragma("unroll") for (int i_ = 0; i_ < 2; ++i_) vAn[h_][i_] = vA[h_][i_]; } } const char* nB = has_next ? (const char*)g.Bt + (size_t)nxt.pb * tstep : cB;
; #pragma nounroll
;         for (int t = 0; t < nt; t += 2) {
;             const bool last = (t == nt - 2);
;             const char* a1 = cA + (size_t)(t + 1) * kstep;
;             const char* a2 = last ? nA : cA + (size_t)(t + 2) * kstep; const char* b2 = last ? nB : cB + (size_t)(t + 2) * kstep;
;             const char* a3 = a2 + kstep; const char* b3 = b2 + kstep;
;             if (last && has_next) S.a_ready(nxt);
;             if constexpr (SP2) {
;             PG8_LDB(B0, 0, 0); PG8_LDB(B1, 0, 1); PG8_SCHED; PG8_LDA(At, 0, 0); PG8_STAGE_A(PG8_SA(1, 1), a1, 1, false);
;             PG8_WAIT_V(8); PG8_WAIT_L(0); PG8_BAR; PG8_MMA(0, 0, At, B0); PG8_MMA(0, 1, At, B1); PG8_BAR; PG8_SCHED;
;             PG8_LDA(At, 0, 1); PG8_STAGE(PG8_SB(0, 0), b2, voffB); PG8_STAGE(PG8_SB(0, 1), b2 + hstepB, voffB); PG8_STAGE_A(PG8_SA(0, 0), a2, 0, last);
;             PG8_WAIT_V(8); PG8_WAIT_L(0); PG8_BAR; PG8_MMA(1, 0, At, B0); PG8_MMA(1, 1, At, B1); PG8_BAR; PG8_SCHED;
.LBB0_1025:
	s_ashr_i32 s45, s44, 31
	s_lshl_b64 s[46:47], s[44:45], 18
	s_add_u32 s46, s88, s46
	s_addc_u32 s47, s89, s47
	s_and_b64 s[48:49], s[2:3], exec
	s_cselect_b32 s5, s47, s7
	s_cselect_b32 s33, s46, s6
	s_ashr_i32 s43, s42, 31
	s_lshl_b64 s[48:49], s[42:43], 18
	v_readlane_b32 s54, v254, 55
	v_readlane_b32 s55, v254, 56
	s_add_u32 s48, s54, s48
	s_addc_u32 s49, s55, s49
	s_and_b64 s[54:55], s[2:3], exec
	s_cselect_b32 s43, s49, s53
	s_cselect_b32 s45, s48, s52
	s_add_u32 s6, s6, 0x20080
	s_addc_u32 s7, s7, 0
	s_add_u32 s71, s52, 0x100
	s_addc_u32 s72, s53, 0
	s_mov_b32 s73, -2
	ds_read_b128 v[26:29], v188
	ds_read_b128 v[30:33], v188 offset:1024
	ds_read_b128 v[18:21], v188 offset:2048
	ds_read_b128 v[22:25], v188 offset:3072
	ds_read_b128 v[10:13], v189
	ds_read_b128 v[14:17], v189 offset:1024
	ds_read_b128 v[2:5], v189 offset:2048
	ds_read_b128 v[6:9], v189 offset:3072
	s_add_u32 s52, s6, 0xfffe0080
	s_addc_u32 s53, s7, -1
	s_cmp_eq_u32 s73, 4
	s_cselect_b32 s55, s5, s53
	s_cselect_b32 s54, s33, s52
	s_cselect_b32 s53, s43, s72
	s_cselect_b32 s52, s45, s71
	v_lshl_add_u64 v[220:221], s[6:7], 0, v[170:171]
	s_add_i32 m0, s51, 0xc000
	ds_read_b128 v[178:181], v190
	ds_read_b128 v[182:185], v190 offset:1024
	ds_read_b128 v[196:199], v190 offset:2048
	ds_read_b128 v[200:203], v190 offset:3072
	ds_read_b128 v[204:207], v190 offset:4096
	ds_read_b128 v[208:211], v190 offset:5120
	ds_read_b128 v[212:215], v190 offset:6144
	ds_read_b128 v[216:219], v190 offset:7168
	global_load_lds_dwordx4 v[220:221], off
	v_lshl_add_u64 v[220:221], s[6:7], 0, v[172:173]
	s_add_i32 m0, s51, 0xe000
	s_nop 0
	global_load_lds_dwordx4 v[220:221], off
	s_waitcnt vmcnt(8)
	s_waitcnt lgkmcnt(0)
	s_barrier
	s_setprio 1
	s_nop 3
	s_waitcnt lgkmcnt(0)
	v_mfma_scale_f32_16x16x128_f8f6f4 v[158:161], v[26:33], v[178:185], 0, v191, v192 op_sel_hi:[0,0,0]
	v_mfma_scale_f32_16x16x128_f8f6f4 v[154:157], v[18:25], v[178:185], 0, v191, v192 op_sel_hi:[0,0,0]
	v_mfma_scale_f32_16x16x128_f8f6f4 v[142:145], v[26:33], v[196:203], 0, v191, v192 op_sel_hi:[0,0,0]
	v_mfma_scale_f32_16x16x128_f8f6f4 v[138:141], v[18:25], v[196:203], 0, v191, v192 op_sel_hi:[0,0,0]
	v_mfma_scale_f32_16x16x128_f8f6f4 v[126:129], v[26:33], v[204:211], 0, v191, v192 op_sel_hi:[0,0,0]
	v_mfma_scale_f32_16x16x128_f8f6f4 v[122:125], v[18:25], v[204:211], 0, v191, v192 op_sel_hi:[0,0,0]
	v_mfma_scale_f32_16x16x128_f8f6f4 v[110:113], v[26:33], v[212:219], 0, v191, v192 op_sel_hi:[0,0,0]
	v_mfma_scale_f32_16x16x128_f8f6f4 v[106:109], v[18:25], v[212:219], 0, v191, v192 op_sel_hi:[0,0,0]
	s_setprio 0
	s_setprio 1
	s_nop 3
	v_mfma_scale_f32_16x16x128_f8f6f4 v[150:153], v[10:17], v[178:185], 0, v191, v192 op_sel_hi:[0,0,0]
	v_mfma_scale_f32_16x16x128_f8f6f4 v[146:149], v[2:9], v[178:185], 0, v191, v192 op_sel_hi:[0,0,0]
	v_mfma_scale_f32_16x16x128_f8f6f4 v[134:137], v[10:17], v[196:203], 0, v191, v192 op_sel_hi:[0,0,0]
	v_mfma_scale_f32_16x16x128_f8f6f4 v[130:133], v[2:9], v[196:203], 0, v191, v192 op_sel_hi:[0,0,0]
	v_mfma_scale_f32_16x16x128_f8f6f4 v[118:121], v[10:17], v[204:211], 0, v191, v192 op_sel_hi:[0,0,0]
	v_mfma_scale_f32_16x16x128_f8f6f4 v[114:117], v[2:9], v[204:211], 0, v191, v192 op_sel_hi:[0,0,0]
	v_mfma_scale_f32_16x16x128_f8f6f4 v[102:105], v[10:17], v[212:219], 0, v191, v192 op_sel_hi:[0,0,0]
	v_mfma_scale_f32_16x16x128_f8f6f4 v[98:101], v[2:9], v[212:219], 0, v191, v192 op_sel_hi:[0,0,0]
	s_setprio 0
	s_barrier
	s_add_i32 s74, s67, s56
	v_lshl_add_u64 v[178:179], s[52:53], 0, v[164:165]
	s_mov_b32 m0, s74
	ds_read_b128 v[196:199], v190 offset:16384
	ds_read_b128 v[200:203], v190 offset:17408
	ds_read_b128 v[204:207], v190 offset:18432
	ds_read_b128 v[208:211], v190 offset:19456
	ds_read_b128 v[212:215], v190 offset:20480
	ds_read_b128 v[216:219], v190 offset:21504
	ds_read_b128 v[220:223], v190 offset:22528
	ds_read_b128 v[224:227], v190 offset:23552
	global_load_lds_dwordx4 v[178:179], off
	s_add_i32 m0, s74, 0x2000
	s_add_u32 s74, s52, 0x8000
	v_lshl_add_u64 v[180:181], s[52:53], 0, v[168:169]
	s_addc_u32 s75, s53, 0
	s_add_i32 s76, s68, s56
	global_load_lds_dwordx4 v[180:181], off
	v_lshl_add_u64 v[182:183], s[74:75], 0, v[164:165]
	s_mov_b32 m0, s76
	v_lshl_add_u64 v[184:185], s[54:55], 0, v[166:167]
	global_load_lds_dwordx4 v[182:183], off
	v_lshl_add_u64 v[182:183], s[74:75], 0, v[168:169]
	s_add_i32 m0, s76, 0x2000
	s_nop 0
	global_load_lds_dwordx4 v[182:183], off
	v_lshl_add_u64 v[182:183], s[54:55], 0, v[162:163]
	s_mov_b32 m0, s51
	s_nop 0
	global_load_lds_dwordx4 v[182:183], off
	s_mov_b32 m0, s57
	s_nop 0
	global_load_lds_dwordx4 v[184:185], off
	s_waitcnt vmcnt(8)
	s_waitcnt lgkmcnt(0)
	s_barrier
	s_setprio 1
	s_nop 3
	s_waitcnt lgkmcnt(0)
	v_mfma_scale_f32_16x16x128_f8f6f4 v[94:97], v[26:33], v[196:203], 0, v191, v192 op_sel_hi:[0,0,0]
	v_mfma_scale_f32_16x16x128_f8f6f4 v[90:93], v[18:25], v[196:203], 0, v191, v192 op_sel_hi:[0,0,0]
	v_mfma_scale_f32_16x16x128_f8f6f4 v[78:81], v[26:33], v[204:211], 0, v191, v192 op_sel_hi:[0,0,0]
	v_mfma_scale_f32_16x16x128_f8f6f4 v[74:77], v[18:25], v[204:211], 0, v191, v192 op_sel_hi:[0,0,0]
	v_mfma_scale_f32_16x16x128_f8f6f4 v[62:65], v[26:33], v[212:219], 0, v191, v192 op_sel_hi:[0,0,0]
	v_mfma_scale_f32_16x16x128_f8f6f4 v[58:61], v[18:25], v[212:219], 0, v191, v192 op_sel_hi:[0,0,0]
	v_mfma_scale_f32_16x16x128_f8f6f4 v[46:49], v[26:33], v[220:227], 0, v191, v192 op_sel_hi:[0,0,0]
	v_mfma_scale_f32_16x16x128_f8f6f4 v[42:45], v[18:25], v[220:227], 0, v191, v192 op_sel_hi:[0,0,0]
	s_setprio 0
	s_setprio 1
	s_nop 3
	v_mfma_scale_f32_16x16x128_f8f6f4 v[86:89], v[10:17], v[196:203], 0, v191, v192 op_sel_hi:[0,0,0]
	v_mfma_scale_f32_16x16x128_f8f6f4 v[82:85], v[2:9], v[196:203], 0, v191, v192 op_sel_hi:[0,0,0]
	v_mfma_scale_f32_16x16x128_f8f6f4 v[70:73], v[10:17], v[204:211], 0, v191, v192 op_sel_hi:[0,0,0]
	v_mfma_scale_f32_16x16x128_f8f6f4 v[66:69], v[2:9], v[204:211], 0, v191, v192 op_sel_hi:[0,0,0]
	v_mfma_scale_f32_16x16x128_f8f6f4 v[54:57], v[10:17], v[212:219], 0, v191, v192 op_sel_hi:[0,0,0]
	v_mfma_scale_f32_16x16x128_f8f6f4 v[50:53], v[2:9], v[212:219], 0, v191, v192 op_sel_hi:[0,0,0]
	v_mfma_scale_f32_16x16x128_f8f6f4 v[38:41], v[10:17], v[220:227], 0, v191, v192 op_sel_hi:[0,0,0]
	v_mfma_scale_f32_16x16x128_f8f6f4 v[34:37], v[2:9], v[220:227], 0, v191, v192 op_sel_hi:[0,0,0]
	s_setprio 0
	s_barrier
; #define PG8_STAGE(bufoff, gbase, voff) do { _Pragma("unroll") for (int _i = 0; _i < 2; ++_i) \
;         __builtin_amdgcn_global_load_lds((const unsigned*)((const char*)(gbase) + (voff)[_i]), (PG8_LAS unsigned*)(lds + (bufoff) + ldsw + _i * 8192), 16, 0, 0); } while (0)
; #define PG8_STAGE_A(bufoff, gbase, h, nx) do { if constexpr (Sched::GATHER) { const unsigned vv_[2] = {(nx) ? vAn[h][0] : vA[h][0], (nx) ? vAn[h][1] : vA[h][1]}; PG8_STAGE(bufoff, gbase, vv_); } \
;         else { PG8_STAGE(bufoff, (gbase) + (h) * hstep, voffA); } } while (0)
; #define PG8_LDA(dst, b, h) do { _Pragma("unroll") for (int m = 0; m < 4; ++m) _Pragma("unroll") for (int k = 0; k < 2; ++k) dst[m][k] = *(const PG8_LAS bf16x8*)(lds + PG8_SA(b, h) + aoff + m * 2048 + k * 1024); } while (0)
; #define PG8_LDB(dst, b, h) do { _Pragma("unroll") for (int n = 0; n < 2; ++n) _Pragma("unroll") for (int k = 0; k < 2; ++k) dst[n][k] = *(const PG8_LAS bf16x8*)(lds + PG8_SB(b, h) + boff + n * 2048 + k * 1024); } while (0)
; #define PG8_WAIT_V(n) asm volatile("s_waitcnt vmcnt(" #n ")" ::: "memory")
; #define PG8_WAIT_L(n) asm volatile("s_waitcnt lgkmcnt(" #n ")" ::: "memory")
; #define PG8_BAR __builtin_amdgcn_s_barrier()
; #define PG8_SCHED __builtin_amdgcn_sched_barrier(0)
;     ...
;             PG8_LDB(B0, 1, 0); PG8_LDB(B1, 1, 1); PG8_SCHED; PG8_LDA(At, 1, 0); PG8_STAGE_A(PG8_SA(0, 1), a2, 1, last);
;             PG8_WAIT_V(8); PG8_WAIT_L(0); PG8_BAR; PG8_MMA(0, 0, At, B0); PG8_MMA(0, 1, At, B1); PG8_BAR; PG8_SCHED;
;             PG8_LDA(At, 1, 1); PG8_STAGE(PG8_SB(1, 0), b3, voffB); PG8_STAGE(PG8_SB(1, 1), b3 + hstepB, voffB); PG8_STAGE_A(PG8_SA(1, 0), a3, 0, last);
;             PG8_WAIT_V(8); PG8_WAIT_L(0); PG8_BAR; PG8_MMA(1, 0, At, B0); PG8_MMA(1, 1, At, B1); PG8_BAR; PG8_SCHED;
	s_add_i32 s74, 0, 0x18000
	s_add_i32 s75, 0, 0x1c000
	v_add_u32_e32 v14, s74, v187
	v_add_u32_e32 v30, s75, v187
	ds_read_b128 v[2:5], v14
	ds_read_b128 v[6:9], v14 offset:1024
	ds_read_b128 v[10:13], v14 offset:2048
	ds_read_b128 v[14:17], v14 offset:3072
	ds_read_b128 v[18:21], v30
	ds_read_b128 v[22:25], v30 offset:1024
	ds_read_b128 v[26:29], v30 offset:2048
	ds_read_b128 v[30:33], v30 offset:3072
	s_add_u32 s54, s54, 0x20000
	s_addc_u32 s55, s55, 0
	s_mov_b32 m0, s58
	v_lshl_add_u64 v[228:229], s[54:55], 0, v[162:163]
	ds_read_b128 v[196:199], v190 offset:32768
	ds_read_b128 v[200:203], v190 offset:33792
	ds_read_b128 v[204:207], v190 offset:34816
	ds_read_b128 v[208:211], v190 offset:35840
	ds_read_b128 v[212:215], v190 offset:36864
	ds_read_b128 v[216:219], v190 offset:37888
	ds_read_b128 v[220:223], v190 offset:38912
	ds_read_b128 v[224:227], v190 offset:39936
	global_load_lds_dwordx4 v[228:229], off
	v_lshl_add_u64 v[228:229], s[54:55], 0, v[166:167]
	s_mov_b32 m0, s59
	s_nop 0
	global_load_lds_dwordx4 v[228:229], off
	s_waitcnt vmcnt(8)
	s_waitcnt lgkmcnt(0)
	s_barrier
	s_setprio 1
	s_nop 3
	s_waitcnt lgkmcnt(0)
	v_mfma_scale_f32_16x16x128_f8f6f4 v[158:161], v[2:9], v[196:203], v[158:161], v191, v192 op_sel_hi:[0,0,0]
	v_mfma_scale_f32_16x16x128_f8f6f4 v[154:157], v[10:17], v[196:203], v[154:157], v191, v192 op_sel_hi:[0,0,0]
	v_mfma_scale_f32_16x16x128_f8f6f4 v[142:145], v[2:9], v[204:211], v[142:145], v191, v192 op_sel_hi:[0,0,0]
	v_mfma_scale_f32_16x16x128_f8f6f4 v[138:141], v[10:17], v[204:211], v[138:141], v191, v192 op_sel_hi:[0,0,0]
	v_mfma_scale_f32_16x16x128_f8f6f4 v[126:129], v[2:9], v[212:219], v[126:129], v191, v192 op_sel_hi:[0,0,0]
	v_mfma_scale_f32_16x16x128_f8f6f4 v[122:125], v[10:17], v[212:219], v[122:125], v191, v192 op_sel_hi:[0,0,0]
	v_mfma_scale_f32_16x16x128_f8f6f4 v[110:113], v[2:9], v[220:227], v[110:113], v191, v192 op_sel_hi:[0,0,0]
	v_mfma_scale_f32_16x16x128_f8f6f4 v[106:109], v[10:17], v[220:227], v[106:109], v191, v192 op_sel_hi:[0,0,0]
	s_setprio 0
	s_setprio 1
	s_nop 3
	v_mfma_scale_f32_16x16x128_f8f6f4 v[150:153], v[18:25], v[196:203], v[150:153], v191, v192 op_sel_hi:[0,0,0]
	v_mfma_scale_f32_16x16x128_f8f6f4 v[146:149], v[26:33], v[196:203], v[146:149], v191, v192 op_sel_hi:[0,0,0]
	v_mfma_scale_f32_16x16x128_f8f6f4 v[134:137], v[18:25], v[204:211], v[134:137], v191, v192 op_sel_hi:[0,0,0]
	v_mfma_scale_f32_16x16x128_f8f6f4 v[130:133], v[26:33], v[204:211], v[130:133], v191, v192 op_sel_hi:[0,0,0]
	v_mfma_scale_f32_16x16x128_f8f6f4 v[118:121], v[18:25], v[212:219], v[118:121], v191, v192 op_sel_hi:[0,0,0]
	v_mfma_scale_f32_16x16x128_f8f6f4 v[114:117], v[26:33], v[212:219], v[114:117], v191, v192 op_sel_hi:[0,0,0]
	v_mfma_scale_f32_16x16x128_f8f6f4 v[102:105], v[18:25], v[220:227], v[102:105], v191, v192 op_sel_hi:[0,0,0]
	v_mfma_scale_f32_16x16x128_f8f6f4 v[98:101], v[26:33], v[220:227], v[98:101], v191, v192 op_sel_hi:[0,0,0]
	s_setprio 0
	s_barrier
	s_add_i32 s54, s74, s56
	v_lshl_add_u64 v[178:179], v[178:179], 0, s[18:19]
	s_mov_b32 m0, s54
	ds_read_b128 v[196:199], v190 offset:49152
	ds_read_b128 v[200:203], v190 offset:50176
	ds_read_b128 v[204:207], v190 offset:51200
	ds_read_b128 v[208:211], v190 offset:52224
	ds_read_b128 v[212:215], v190 offset:53248
	ds_read_b128 v[216:219], v190 offset:54272
	ds_read_b128 v[220:223], v190 offset:55296
	ds_read_b128 v[224:227], v190 offset:56320
	global_load_lds_dwordx4 v[178:179], off
	s_add_i32 m0, s54, 0x2000
	s_add_u32 s52, s52, 0x8080
	v_lshl_add_u64 v[178:179], v[180:181], 0, s[18:19]
	s_addc_u32 s53, s53, 0
	s_add_i32 s54, s75, s56
	global_load_lds_dwordx4 v[178:179], off
	v_lshl_add_u64 v[178:179], s[52:53], 0, v[164:165]
	s_mov_b32 m0, s54
	s_nop 0
	global_load_lds_dwordx4 v[178:179], off
	v_lshl_add_u64 v[178:179], s[52:53], 0, v[168:169]
	s_add_i32 m0, s54, 0x2000
	s_nop 0
	global_load_lds_dwordx4 v[178:179], off
	v_lshl_add_u64 v[178:179], v[182:183], 0, s[18:19]
	s_mov_b32 m0, s64
	s_nop 0
	global_load_lds_dwordx4 v[178:179], off
	v_lshl_add_u64 v[178:179], v[184:185], 0, s[18:19]
	s_mov_b32 m0, s65
	s_nop 0
	global_load_lds_dwordx4 v[178:179], off
	s_waitcnt vmcnt(8)
	s_waitcnt lgkmcnt(0)
	s_barrier
	s_setprio 1
	s_nop 3
	s_waitcnt lgkmcnt(0)
	v_mfma_scale_f32_16x16x128_f8f6f4 v[94:97], v[2:9], v[196:203], v[94:97], v191, v192 op_sel_hi:[0,0,0]
	v_mfma_scale_f32_16x16x128_f8f6f4 v[90:93], v[10:17], v[196:203], v[90:93], v191, v192 op_sel_hi:[0,0,0]
	v_mfma_scale_f32_16x16x128_f8f6f4 v[78:81], v[2:9], v[204:211], v[78:81], v191, v192 op_sel_hi:[0,0,0]
	v_mfma_scale_f32_16x16x128_f8f6f4 v[74:77], v[10:17], v[204:211], v[74:77], v191, v192 op_sel_hi:[0,0,0]
	v_mfma_scale_f32_16x16x128_f8f6f4 v[62:65], v[2:9], v[212:219], v[62:65], v191, v192 op_sel_hi:[0,0,0]
	v_mfma_scale_f32_16x16x128_f8f6f4 v[58:61], v[10:17], v[212:219], v[58:61], v191, v192 op_sel_hi:[0,0,0]
	v_mfma_scale_f32_16x16x128_f8f6f4 v[46:49], v[2:9], v[220:227], v[46:49], v191, v192 op_sel_hi:[0,0,0]
	v_mfma_scale_f32_16x16x128_f8f6f4 v[42:45], v[10:17], v[220:227], v[42:45], v191, v192 op_sel_hi:[0,0,0]
	s_setprio 0
	s_setprio 1
	s_nop 3
	v_mfma_scale_f32_16x16x128_f8f6f4 v[86:89], v[18:25], v[196:203], v[86:89], v191, v192 op_sel_hi:[0,0,0]
	v_mfma_scale_f32_16x16x128_f8f6f4 v[82:85], v[26:33], v[196:203], v[82:85], v191, v192 op_sel_hi:[0,0,0]
	v_mfma_scale_f32_16x16x128_f8f6f4 v[70:73], v[18:25], v[204:211], v[70:73], v191, v192 op_sel_hi:[0,0,0]
	v_mfma_scale_f32_16x16x128_f8f6f4 v[66:69], v[26:33], v[204:211], v[66:69], v191, v192 op_sel_hi:[0,0,0]
	v_mfma_scale_f32_16x16x128_f8f6f4 v[54:57], v[18:25], v[212:219], v[54:57], v191, v192 op_sel_hi:[0,0,0]
	v_mfma_scale_f32_16x16x128_f8f6f4 v[50:53], v[26:33], v[212:219], v[50:53], v191, v192 op_sel_hi:[0,0,0]
	v_mfma_scale_f32_16x16x128_f8f6f4 v[38:41], v[18:25], v[220:227], v[38:41], v191, v192 op_sel_hi:[0,0,0]
	v_mfma_scale_f32_16x16x128_f8f6f4 v[34:37], v[26:33], v[220:227], v[34:37], v191, v192 op_sel_hi:[0,0,0]
	s_setprio 0
	s_barrier
	s_add_i32 s73, s73, 2
	s_add_u32 s6, s6, 0x100
	s_addc_u32 s7, s7, 0
	s_add_u32 s71, s71, 0x100
	s_addc_u32 s72, s72, 0
; #define PG8_STAGE(bufoff, gbase, voff) do { _Pragma("unroll") for (int _i = 0; _i < 2; ++_i) \
;         __builtin_amdgcn_global_load_lds((const unsigned*)((const char*)(gbase) + (voff)[_i]), (PG8_LAS unsigned*)(lds + (bufoff) + ldsw + _i * 8192), 16, 0, 0); } while (0)
; #define PG8_STAGE_A(bufoff, gbase, h, nx) do { if constexpr (Sched::GATHER) { const unsigned vv_[2] = {(nx) ? vAn[h][0] : vA[h][0], (nx) ? vAn[h][1] : vA[h][1]}; PG8_STAGE(bufoff, gbase, vv_); } \
;         else { PG8_STAGE(bufoff, (gbase) + (h) * hstep, voffA); } } while (0)
; #define PG8_LDA(dst, b, h) do { _Pragma("unroll") for (int m = 0; m < 4; ++m) _Pragma("unroll") for (int k = 0; k < 2; ++k) dst[m][k] = *(const PG8_LAS bf16x8*)(lds + PG8_SA(b, h) + aoff + m * 2048 + k * 1024); } while (0)
; #define PG8_LDB(dst, b, h) do { _Pragma("unroll") for (int n = 0; n < 2; ++n) _Pragma("unroll") for (int k = 0; k < 2; ++k) dst[n][k] = *(const PG8_LAS bf16x8*)(lds + PG8_SB(b, h) + boff + n * 2048 + k * 1024); } while (0)
; #define PG8_WAIT_V(n) asm volatile("s_waitcnt vmcnt(" #n ")" ::: "memory")
; #define PG8_WAIT_L(n) asm volatile("s_waitcnt lgkmcnt(" #n ")" ::: "memory")
; #define PG8_BAR __builtin_amdgcn_s_barrier()
; #define PG8_SCHED __builtin_amdgcn_sched_barrier(0)
;     ...
;             PG8_LDB(B0, 0, 0); PG8_LDB(B1, 0, 1); PG8_SCHED; PG8_LDA(At, 0, 0); PG8_STAGE_A(PG8_SA(1, 1), a1, 1, false);
;             PG8_WAIT_V(8); PG8_WAIT_L(0); PG8_BAR; PG8_MMA(0, 0, At, B0); PG8_MMA(0, 1, At, B1); PG8_BAR; PG8_SCHED;
;             PG8_LDA(At, 0, 1); PG8_STAGE(PG8_SB(0, 0), b2, voffB); PG8_STAGE(PG8_SB(0, 1), b2 + hstepB, voffB); PG8_STAGE_A(PG8_SA(0, 0), a2, 0, last);
;             PG8_WAIT_V(8); PG8_WAIT_L(0); PG8_BAR; PG8_MMA(1, 0, At, B0); PG8_MMA(1, 1, At, B1); PG8_BAR; PG8_SCHED;
.LBB0_1026:
	ds_read_b128 v[26:29], v188
	ds_read_b128 v[30:33], v188 offset:1024
	ds_read_b128 v[18:21], v188 offset:2048
	ds_read_b128 v[22:25], v188 offset:3072
	ds_read_b128 v[10:13], v189
	ds_read_b128 v[14:17], v189 offset:1024
	ds_read_b128 v[2:5], v189 offset:2048
	ds_read_b128 v[6:9], v189 offset:3072
	s_add_u32 s52, s6, 0xfffe0080
	s_addc_u32 s53, s7, -1
	s_cmp_eq_u32 s73, 4
	s_cselect_b32 s55, s5, s53
	s_cselect_b32 s54, s33, s52
	s_cselect_b32 s53, s43, s72
	s_cselect_b32 s52, s45, s71
	v_lshl_add_u64 v[220:221], s[6:7], 0, v[170:171]
	s_add_i32 m0, s51, 0xc000
	ds_read_b128 v[178:181], v190
	ds_read_b128 v[182:185], v190 offset:1024
	ds_read_b128 v[196:199], v190 offset:2048
	ds_read_b128 v[200:203], v190 offset:3072
	ds_read_b128 v[204:207], v190 offset:4096
	ds_read_b128 v[208:211], v190 offset:5120
	ds_read_b128 v[212:215], v190 offset:6144
	ds_read_b128 v[216:219], v190 offset:7168
	global_load_lds_dwordx4 v[220:221], off
	v_lshl_add_u64 v[220:221], s[6:7], 0, v[172:173]
	s_add_i32 m0, s51, 0xe000
	s_nop 0
	global_load_lds_dwordx4 v[220:221], off
	s_waitcnt vmcnt(8)
	s_waitcnt lgkmcnt(0)
	s_barrier
	s_setprio 1
	s_nop 3
	s_waitcnt lgkmcnt(0)
	v_mfma_scale_f32_16x16x128_f8f6f4 v[158:161], v[26:33], v[178:185], v[158:161], v191, v192 op_sel_hi:[0,0,0]
	v_mfma_scale_f32_16x16x128_f8f6f4 v[154:157], v[18:25], v[178:185], v[154:157], v191, v192 op_sel_hi:[0,0,0]
	v_mfma_scale_f32_16x16x128_f8f6f4 v[142:145], v[26:33], v[196:203], v[142:145], v191, v192 op_sel_hi:[0,0,0]
	v_mfma_scale_f32_16x16x128_f8f6f4 v[138:141], v[18:25], v[196:203], v[138:141], v191, v192 op_sel_hi:[0,0,0]
	v_mfma_scale_f32_16x16x128_f8f6f4 v[126:129], v[26:33], v[204:211], v[126:129], v191, v192 op_sel_hi:[0,0,0]
	v_mfma_scale_f32_16x16x128_f8f6f4 v[122:125], v[18:25], v[204:211], v[122:125], v191, v192 op_sel_hi:[0,0,0]
	v_mfma_scale_f32_16x16x128_f8f6f4 v[110:113], v[26:33], v[212:219], v[110:113], v191, v192 op_sel_hi:[0,0,0]
	v_mfma_scale_f32_16x16x128_f8f6f4 v[106:109], v[18:25], v[212:219], v[106:109], v191, v192 op_sel_hi:[0,0,0]
	s_setprio 0
	s_setprio 1
	s_nop 3
	v_mfma_scale_f32_16x16x128_f8f6f4 v[150:153], v[10:17], v[178:185], v[150:153], v191, v192 op_sel_hi:[0,0,0]
	v_mfma_scale_f32_16x16x128_f8f6f4 v[146:149], v[2:9], v[178:185], v[146:149], v191, v192 op_sel_hi:[0,0,0]
	v_mfma_scale_f32_16x16x128_f8f6f4 v[134:137], v[10:17], v[196:203], v[134:137], v191, v192 op_sel_hi:[0,0,0]
	v_mfma_scale_f32_16x16x128_f8f6f4 v[130:133], v[2:9], v[196:203], v[130:133], v191, v192 op_sel_hi:[0,0,0]
	v_mfma_scale_f32_16x16x128_f8f6f4 v[118:121], v[10:17], v[204:211], v[118:121], v191, v192 op_sel_hi:[0,0,0]
	v_mfma_scale_f32_16x16x128_f8f6f4 v[114:117], v[2:9], v[204:211], v[114:117], v191, v192 op_sel_hi:[0,0,0]
	v_mfma_scale_f32_16x16x128_f8f6f4 v[102:105], v[10:17], v[212:219], v[102:105], v191, v192 op_sel_hi:[0,0,0]
	v_mfma_scale_f32_16x16x128_f8f6f4 v[98:101], v[2:9], v[212:219], v[98:101], v191, v192 op_sel_hi:[0,0,0]
	s_setprio 0
	s_barrier
	s_add_i32 s74, s67, s56
	v_lshl_add_u64 v[178:179], s[52:53], 0, v[164:165]
	s_mov_b32 m0, s74
	ds_read_b128 v[196:199], v190 offset:16384
	ds_read_b128 v[200:203], v190 offset:17408
	ds_read_b128 v[204:207], v190 offset:18432
	ds_read_b128 v[208:211], v190 offset:19456
	ds_read_b128 v[212:215], v190 offset:20480
	ds_read_b128 v[216:219], v190 offset:21504
	ds_read_b128 v[220:223], v190 offset:22528
	ds_read_b128 v[224:227], v190 offset:23552
	global_load_lds_dwordx4 v[178:179], off
	s_add_i32 m0, s74, 0x2000
	s_add_u32 s74, s52, 0x8000
	v_lshl_add_u64 v[180:181], s[52:53], 0, v[168:169]
	s_addc_u32 s75, s53, 0
	s_add_i32 s76, s68, s56
	global_load_lds_dwordx4 v[180:181], off
	v_lshl_add_u64 v[182:183], s[74:75], 0, v[164:165]
	s_mov_b32 m0, s76
	v_lshl_add_u64 v[184:185], s[54:55], 0, v[166:167]
	global_load_lds_dwordx4 v[182:183], off
	v_lshl_add_u64 v[182:183], s[74:75], 0, v[168:169]
	s_add_i32 m0, s76, 0x2000
	s_nop 0
	global_load_lds_dwordx4 v[182:183], off
	v_lshl_add_u64 v[182:183], s[54:55], 0, v[162:163]
	s_mov_b32 m0, s51
	s_nop 0
	global_load_lds_dwordx4 v[182:183], off
	s_mov_b32 m0, s57
	s_nop 0
	global_load_lds_dwordx4 v[184:185], off
	s_waitcnt vmcnt(8)
	s_waitcnt lgkmcnt(0)
	s_barrier
	s_setprio 1
	s_nop 3
	s_waitcnt lgkmcnt(0)
	v_mfma_scale_f32_16x16x128_f8f6f4 v[94:97], v[26:33], v[196:203], v[94:97], v191, v192 op_sel_hi:[0,0,0]
	v_mfma_scale_f32_16x16x128_f8f6f4 v[90:93], v[18:25], v[196:203], v[90:93], v191, v192 op_sel_hi:[0,0,0]
	v_mfma_scale_f32_16x16x128_f8f6f4 v[78:81], v[26:33], v[204:211], v[78:81], v191, v192 op_sel_hi:[0,0,0]
	v_mfma_scale_f32_16x16x128_f8f6f4 v[74:77], v[18:25], v[204:211], v[74:77], v191, v192 op_sel_hi:[0,0,0]
	v_mfma_scale_f32_16x16x128_f8f6f4 v[62:65], v[26:33], v[212:219], v[62:65], v191, v192 op_sel_hi:[0,0,0]
	v_mfma_scale_f32_16x16x128_f8f6f4 v[58:61], v[18:25], v[212:219], v[58:61], v191, v192 op_sel_hi:[0,0,0]
	v_mfma_scale_f32_16x16x128_f8f6f4 v[46:49], v[26:33], v[220:227], v[46:49], v191, v192 op_sel_hi:[0,0,0]
	v_mfma_scale_f32_16x16x128_f8f6f4 v[42:45], v[18:25], v[220:227], v[42:45], v191, v192 op_sel_hi:[0,0,0]
	s_setprio 0
	s_setprio 1
	s_nop 3
	v_mfma_scale_f32_16x16x128_f8f6f4 v[86:89], v[10:17], v[196:203], v[86:89], v191, v192 op_sel_hi:[0,0,0]
	v_mfma_scale_f32_16x16x128_f8f6f4 v[82:85], v[2:9], v[196:203], v[82:85], v191, v192 op_sel_hi:[0,0,0]
	v_mfma_scale_f32_16x16x128_f8f6f4 v[70:73], v[10:17], v[204:211], v[70:73], v191, v192 op_sel_hi:[0,0,0]
	v_mfma_scale_f32_16x16x128_f8f6f4 v[66:69], v[2:9], v[204:211], v[66:69], v191, v192 op_sel_hi:[0,0,0]
	v_mfma_scale_f32_16x16x128_f8f6f4 v[54:57], v[10:17], v[212:219], v[54:57], v191, v192 op_sel_hi:[0,0,0]
	v_mfma_scale_f32_16x16x128_f8f6f4 v[50:53], v[2:9], v[212:219], v[50:53], v191, v192 op_sel_hi:[0,0,0]
	v_mfma_scale_f32_16x16x128_f8f6f4 v[38:41], v[10:17], v[220:227], v[38:41], v191, v192 op_sel_hi:[0,0,0]
	v_mfma_scale_f32_16x16x128_f8f6f4 v[34:37], v[2:9], v[220:227], v[34:37], v191, v192 op_sel_hi:[0,0,0]
	s_setprio 0
	s_barrier
; #define PG8_STAGE(bufoff, gbase, voff) do { _Pragma("unroll") for (int _i = 0; _i < 2; ++_i) \
;         __builtin_amdgcn_global_load_lds((const unsigned*)((const char*)(gbase) + (voff)[_i]), (PG8_LAS unsigned*)(lds + (bufoff) + ldsw + _i * 8192), 16, 0, 0); } while (0)
; #define PG8_STAGE_A(bufoff, gbase, h, nx) do { if constexpr (Sched::GATHER) { const unsigned vv_[2] = {(nx) ? vAn[h][0] : vA[h][0], (nx) ? vAn[h][1] : vA[h][1]}; PG8_STAGE(bufoff, gbase, vv_); } \
;         else { PG8_STAGE(bufoff, (gbase) + (h) * hstep, voffA); } } while (0)
; #define PG8_LDA(dst, b, h) do { _Pragma("unroll") for (int m = 0; m < 4; ++m) _Pragma("unroll") for (int k = 0; k < 2; ++k) dst[m][k] = *(const PG8_LAS bf16x8*)(lds + PG8_SA(b, h) + aoff + m * 2048 + k * 1024); } while (0)
; #define PG8_LDB(dst, b, h) do { _Pragma("unroll") for (int n = 0; n < 2; ++n) _Pragma("unroll") for (int k = 0; k < 2; ++k) dst[n][k] = *(const PG8_LAS bf16x8*)(lds + PG8_SB(b, h) + boff + n * 2048 + k * 1024); } while (0)
; #define PG8_WAIT_V(n) asm volatile("s_waitcnt vmcnt(" #n ")" ::: "memory")
; #define PG8_WAIT_L(n) asm volatile("s_waitcnt lgkmcnt(" #n ")" ::: "memory")
; #define PG8_BAR __builtin_amdgcn_s_barrier()
; #define PG8_SCHED __builtin_amdgcn_sched_barrier(0)
;     ...
;             PG8_LDB(B0, 1, 0); PG8_LDB(B1, 1, 1); PG8_SCHED; PG8_LDA(At, 1, 0); PG8_STAGE_A(PG8_SA(0, 1), a2, 1, last);
;             PG8_WAIT_V(8); PG8_WAIT_L(0); PG8_BAR; PG8_MMA(0, 0, At, B0); PG8_MMA(0, 1, At, B1); PG8_BAR; PG8_SCHED;
;             PG8_LDA(At, 1, 1); PG8_STAGE(PG8_SB(1, 0), b3, voffB); PG8_STAGE(PG8_SB(1, 1), b3 + hstepB, voffB); PG8_STAGE_A(PG8_SA(1, 0), a3, 0, last);
;             PG8_WAIT_V(8); PG8_WAIT_L(0); PG8_BAR; PG8_MMA(1, 0, At, B0); PG8_MMA(1, 1, At, B1); PG8_BAR; PG8_SCHED;
;     ...
;         if constexpr (F8) asm volatile("s_nop 15\n\ts_nop 15\n\ts_nop 15" ::: "memory");
	s_add_i32 s74, 0, 0x18000
	s_add_i32 s75, 0, 0x1c000
	v_add_u32_e32 v14, s74, v187
	v_add_u32_e32 v30, s75, v187
	ds_read_b128 v[2:5], v14
	ds_read_b128 v[6:9], v14 offset:1024
	ds_read_b128 v[10:13], v14 offset:2048
	ds_read_b128 v[14:17], v14 offset:3072
	ds_read_b128 v[18:21], v30
	ds_read_b128 v[22:25], v30 offset:1024
	ds_read_b128 v[26:29], v30 offset:2048
	ds_read_b128 v[30:33], v30 offset:3072
	s_add_u32 s54, s54, 0x20000
	s_addc_u32 s55, s55, 0
	s_mov_b32 m0, s58
	v_lshl_add_u64 v[228:229], s[54:55], 0, v[162:163]
	ds_read_b128 v[196:199], v190 offset:32768
	ds_read_b128 v[200:203], v190 offset:33792
	ds_read_b128 v[204:207], v190 offset:34816
	ds_read_b128 v[208:211], v190 offset:35840
	ds_read_b128 v[212:215], v190 offset:36864
	ds_read_b128 v[216:219], v190 offset:37888
	ds_read_b128 v[220:223], v190 offset:38912
	ds_read_b128 v[224:227], v190 offset:39936
	global_load_lds_dwordx4 v[228:229], off
	v_lshl_add_u64 v[228:229], s[54:55], 0, v[166:167]
	s_mov_b32 m0, s59
	s_nop 0
	global_load_lds_dwordx4 v[228:229], off
	s_waitcnt vmcnt(8)
	s_waitcnt lgkmcnt(0)
	s_barrier
	s_setprio 1
	s_nop 3
	s_waitcnt lgkmcnt(0)
	v_mfma_scale_f32_16x16x128_f8f6f4 v[158:161], v[2:9], v[196:203], v[158:161], v191, v192 op_sel_hi:[0,0,0]
	v_mfma_scale_f32_16x16x128_f8f6f4 v[154:157], v[10:17], v[196:203], v[154:157], v191, v192 op_sel_hi:[0,0,0]
	v_mfma_scale_f32_16x16x128_f8f6f4 v[142:145], v[2:9], v[204:211], v[142:145], v191, v192 op_sel_hi:[0,0,0]
	v_mfma_scale_f32_16x16x128_f8f6f4 v[138:141], v[10:17], v[204:211], v[138:141], v191, v192 op_sel_hi:[0,0,0]
	v_mfma_scale_f32_16x16x128_f8f6f4 v[126:129], v[2:9], v[212:219], v[126:129], v191, v192 op_sel_hi:[0,0,0]
	v_mfma_scale_f32_16x16x128_f8f6f4 v[122:125], v[10:17], v[212:219], v[122:125], v191, v192 op_sel_hi:[0,0,0]
	v_mfma_scale_f32_16x16x128_f8f6f4 v[110:113], v[2:9], v[220:227], v[110:113], v191, v192 op_sel_hi:[0,0,0]
	v_mfma_scale_f32_16x16x128_f8f6f4 v[106:109], v[10:17], v[220:227], v[106:109], v191, v192 op_sel_hi:[0,0,0]
	s_setprio 0
	s_setprio 1
	s_nop 3
	v_mfma_scale_f32_16x16x128_f8f6f4 v[150:153], v[18:25], v[196:203], v[150:153], v191, v192 op_sel_hi:[0,0,0]
	v_mfma_scale_f32_16x16x128_f8f6f4 v[146:149], v[26:33], v[196:203], v[146:149], v191, v192 op_sel_hi:[0,0,0]
	v_mfma_scale_f32_16x16x128_f8f6f4 v[134:137], v[18:25], v[204:211], v[134:137], v191, v192 op_sel_hi:[0,0,0]
	v_mfma_scale_f32_16x16x128_f8f6f4 v[130:133], v[26:33], v[204:211], v[130:133], v191, v192 op_sel_hi:[0,0,0]
	v_mfma_scale_f32_16x16x128_f8f6f4 v[118:121], v[18:25], v[212:219], v[118:121], v191, v192 op_sel_hi:[0,0,0]
	v_mfma_scale_f32_16x16x128_f8f6f4 v[114:117], v[26:33], v[212:219], v[114:117], v191, v192 op_sel_hi:[0,0,0]
	v_mfma_scale_f32_16x16x128_f8f6f4 v[102:105], v[18:25], v[220:227], v[102:105], v191, v192 op_sel_hi:[0,0,0]
	v_mfma_scale_f32_16x16x128_f8f6f4 v[98:101], v[26:33], v[220:227], v[98:101], v191, v192 op_sel_hi:[0,0,0]
	s_setprio 0
	s_barrier
	s_add_i32 s54, s74, s56
	v_lshl_add_u64 v[178:179], v[178:179], 0, s[18:19]
	s_mov_b32 m0, s54
	ds_read_b128 v[196:199], v190 offset:49152
	ds_read_b128 v[200:203], v190 offset:50176
	ds_read_b128 v[204:207], v190 offset:51200
	ds_read_b128 v[208:211], v190 offset:52224
	ds_read_b128 v[212:215], v190 offset:53248
	ds_read_b128 v[216:219], v190 offset:54272
	ds_read_b128 v[220:223], v190 offset:55296
	ds_read_b128 v[224:227], v190 offset:56320
	global_load_lds_dwordx4 v[178:179], off
	s_add_i32 m0, s54, 0x2000
	s_add_u32 s52, s52, 0x8080
	v_lshl_add_u64 v[178:179], v[180:181], 0, s[18:19]
	s_addc_u32 s53, s53, 0
	s_add_i32 s54, s75, s56
	global_load_lds_dwordx4 v[178:179], off
	v_lshl_add_u64 v[178:179], s[52:53], 0, v[164:165]
	s_mov_b32 m0, s54
	s_nop 0
	global_load_lds_dwordx4 v[178:179], off
	v_lshl_add_u64 v[178:179], s[52:53], 0, v[168:169]
	s_add_i32 m0, s54, 0x2000
	s_nop 0
	global_load_lds_dwordx4 v[178:179], off
	v_lshl_add_u64 v[178:179], v[182:183], 0, s[18:19]
	s_mov_b32 m0, s64
	s_nop 0
	global_load_lds_dwordx4 v[178:179], off
	v_lshl_add_u64 v[178:179], v[184:185], 0, s[18:19]
	s_mov_b32 m0, s65
	s_nop 0
	global_load_lds_dwordx4 v[178:179], off
	s_waitcnt vmcnt(8)
	s_waitcnt lgkmcnt(0)
	s_barrier
	s_setprio 1
	s_nop 3
	s_waitcnt lgkmcnt(0)
	v_mfma_scale_f32_16x16x128_f8f6f4 v[94:97], v[2:9], v[196:203], v[94:97], v191, v192 op_sel_hi:[0,0,0]
	v_mfma_scale_f32_16x16x128_f8f6f4 v[90:93], v[10:17], v[196:203], v[90:93], v191, v192 op_sel_hi:[0,0,0]
	v_mfma_scale_f32_16x16x128_f8f6f4 v[78:81], v[2:9], v[204:211], v[78:81], v191, v192 op_sel_hi:[0,0,0]
	v_mfma_scale_f32_16x16x128_f8f6f4 v[74:77], v[10:17], v[204:211], v[74:77], v191, v192 op_sel_hi:[0,0,0]
	v_mfma_scale_f32_16x16x128_f8f6f4 v[62:65], v[2:9], v[212:219], v[62:65], v191, v192 op_sel_hi:[0,0,0]
	v_mfma_scale_f32_16x16x128_f8f6f4 v[58:61], v[10:17], v[212:219], v[58:61], v191, v192 op_sel_hi:[0,0,0]
	v_mfma_scale_f32_16x16x128_f8f6f4 v[46:49], v[2:9], v[220:227], v[46:49], v191, v192 op_sel_hi:[0,0,0]
	v_mfma_scale_f32_16x16x128_f8f6f4 v[42:45], v[10:17], v[220:227], v[42:45], v191, v192 op_sel_hi:[0,0,0]
	s_setprio 0
	s_setprio 1
	s_nop 3
	v_mfma_scale_f32_16x16x128_f8f6f4 v[86:89], v[18:25], v[196:203], v[86:89], v191, v192 op_sel_hi:[0,0,0]
	v_mfma_scale_f32_16x16x128_f8f6f4 v[82:85], v[26:33], v[196:203], v[82:85], v191, v192 op_sel_hi:[0,0,0]
	v_mfma_scale_f32_16x16x128_f8f6f4 v[70:73], v[18:25], v[204:211], v[70:73], v191, v192 op_sel_hi:[0,0,0]
	v_mfma_scale_f32_16x16x128_f8f6f4 v[66:69], v[26:33], v[204:211], v[66:69], v191, v192 op_sel_hi:[0,0,0]
	v_mfma_scale_f32_16x16x128_f8f6f4 v[54:57], v[18:25], v[212:219], v[54:57], v191, v192 op_sel_hi:[0,0,0]
	v_mfma_scale_f32_16x16x128_f8f6f4 v[50:53], v[26:33], v[212:219], v[50:53], v191, v192 op_sel_hi:[0,0,0]
	v_mfma_scale_f32_16x16x128_f8f6f4 v[38:41], v[18:25], v[220:227], v[38:41], v191, v192 op_sel_hi:[0,0,0]
	v_mfma_scale_f32_16x16x128_f8f6f4 v[34:37], v[26:33], v[220:227], v[34:37], v191, v192 op_sel_hi:[0,0,0]
	s_setprio 0
	s_barrier
	s_add_i32 s73, s73, 2
	s_add_u32 s6, s6, 0x100
	s_addc_u32 s7, s7, 0
	s_add_u32 s71, s71, 0x100
	s_addc_u32 s72, s72, 0
	s_cmp_gt_u32 s73, 5
	s_cbranch_scc0 .LBB0_1026
	s_and_b64 vcc, exec, s[20:21]
	s_cbranch_vccz .LBB0_1029
	s_barrier

; #define PG8_STAGE(bufoff, gbase, voff) do { _Pragma("unroll") for (int _i = 0; _i < 2; ++_i) \
;         __builtin_amdgcn_global_load_lds((const unsigned*)((const char*)(gbase) + (voff)[_i]), (PG8_LAS unsigned*)(lds + (bufoff) + ldsw + _i * 8192), 16, 0, 0); } while (0)
; #define PG8_STAGE_A(bufoff, gbase, h, nx) do { if constexpr (Sched::GATHER) { const unsigned vv_[2] = {(nx) ? vAn[h][0] : vA[h][0], (nx) ? vAn[h][1] : vA[h][1]}; PG8_STAGE(bufoff, gbase, vv_); } \
;         else { PG8_STAGE(bufoff, (gbase) + (h) * hstep, voffA); } } while (0)
; #define PG8_LDA(dst, b, h) do { _Pragma("unroll") for (int m = 0; m < 4; ++m) _Pragma("unroll") for (int k = 0; k < 2; ++k) dst[m][k] = *(const PG8_LAS bf16x8*)(lds + PG8_SA(b, h) + aoff + m * 2048 + k * 1024); } while (0)
; #define PG8_LDB(dst, b, h) do { _Pragma("unroll") for (int n = 0; n < 2; ++n) _Pragma("unroll") for (int k = 0; k < 2; ++k) dst[n][k] = *(const PG8_LAS bf16x8*)(lds + PG8_SB(b, h) + boff + n * 2048 + k * 1024); } while (0)
; #define PG8_WAIT_V(n) asm volatile("s_waitcnt vmcnt(" #n ")" ::: "memory")
; #define PG8_WAIT_L(n) asm volatile("s_waitcnt lgkmcnt(" #n ")" ::: "memory")
; #define PG8_BAR __builtin_amdgcn_s_barrier()
; #define PG8_SCHED __builtin_amdgcn_sched_barrier(0)
;     ...
;             PG8_LDB(B0, 0, 0); PG8_LDB(B1, 0, 1); PG8_SCHED; PG8_LDA(At, 0, 0); PG8_STAGE_A(PG8_SA(1, 1), a1, 1, false);
;             PG8_WAIT_V(8); PG8_WAIT_L(0); PG8_BAR; PG8_MMA(0, 0, At, B0); PG8_MMA(0, 1, At, B1); PG8_BAR; PG8_SCHED;
;             PG8_LDA(At, 0, 1); PG8_STAGE(PG8_SB(0, 0), b2, voffB); PG8_STAGE(PG8_SB(0, 1), b2 + hstepB, voffB); PG8_STAGE_A(PG8_SA(0, 0), a2, 0, last);
;             PG8_WAIT_V(8); PG8_WAIT_L(0); PG8_BAR; PG8_MMA(1, 0, At, B0); PG8_MMA(1, 1, At, B1); PG8_BAR; PG8_SCHED;
.LBB0_1572:
	ds_read_b128 v[26:29], v194
	ds_read_b128 v[30:33], v194 offset:1024
	ds_read_b128 v[18:21], v194 offset:2048
	ds_read_b128 v[22:25], v194 offset:3072
	ds_read_b128 v[10:13], v195
	ds_read_b128 v[14:17], v195 offset:1024
	ds_read_b128 v[2:5], v195 offset:2048
	ds_read_b128 v[6:9], v195 offset:3072
	s_add_u32 s20, s58, s4
	s_addc_u32 s21, s59, s5
	s_add_u32 s22, s20, 0x25400100
	s_addc_u32 s23, s21, 0
	s_add_u32 s55, s52, s4
	s_addc_u32 s56, s53, s5
	s_cmpk_eq_i32 s4, 0x300
	s_cselect_b64 vcc, -1, 0
	s_and_b64 s[20:21], vcc, exec
	s_cselect_b32 s23, s93, s23
	s_cselect_b32 s22, s92, s22
	s_cselect_b32 s21, s17, s56
	s_cselect_b32 s20, s51, s55
	s_mov_b32 m0, s39
	v_lshl_add_u64 v[232:233], v[180:181], 0, s[4:5]
	ds_read_b128 v[182:185], v196
	ds_read_b128 v[186:189], v196 offset:1024
	ds_read_b128 v[208:211], v196 offset:2048
	ds_read_b128 v[212:215], v196 offset:3072
	ds_read_b128 v[216:219], v196 offset:4096
	ds_read_b128 v[220:223], v196 offset:5120
	ds_read_b128 v[224:227], v196 offset:6144
	ds_read_b128 v[228:231], v196 offset:7168
	global_load_lds_dwordx4 v[232:233], off
	v_lshl_add_u64 v[232:233], v[178:179], 0, s[4:5]
	s_mov_b32 m0, s40
	s_nop 0
	global_load_lds_dwordx4 v[232:233], off
	s_waitcnt vmcnt(8)
	s_waitcnt lgkmcnt(0)
	s_barrier
	s_setprio 1
	s_nop 3
	s_waitcnt lgkmcnt(0)
	v_mfma_scale_f32_16x16x128_f8f6f4 v[158:161], v[26:33], v[182:189], v[158:161], v197, v198 op_sel_hi:[0,0,0]
	v_mfma_scale_f32_16x16x128_f8f6f4 v[150:153], v[18:25], v[182:189], v[150:153], v197, v198 op_sel_hi:[0,0,0]
	v_mfma_scale_f32_16x16x128_f8f6f4 v[142:145], v[26:33], v[208:215], v[142:145], v197, v198 op_sel_hi:[0,0,0]
	v_mfma_scale_f32_16x16x128_f8f6f4 v[134:137], v[18:25], v[208:215], v[134:137], v197, v198 op_sel_hi:[0,0,0]
	v_mfma_scale_f32_16x16x128_f8f6f4 v[126:129], v[26:33], v[216:223], v[126:129], v197, v198 op_sel_hi:[0,0,0]
	v_mfma_scale_f32_16x16x128_f8f6f4 v[118:121], v[18:25], v[216:223], v[118:121], v197, v198 op_sel_hi:[0,0,0]
	v_mfma_scale_f32_16x16x128_f8f6f4 v[110:113], v[26:33], v[224:231], v[110:113], v197, v198 op_sel_hi:[0,0,0]
	v_mfma_scale_f32_16x16x128_f8f6f4 v[98:101], v[18:25], v[224:231], v[98:101], v197, v198 op_sel_hi:[0,0,0]
	s_setprio 0
	s_setprio 1
	s_nop 3
	v_mfma_scale_f32_16x16x128_f8f6f4 v[154:157], v[10:17], v[182:189], v[154:157], v197, v198 op_sel_hi:[0,0,0]
	v_mfma_scale_f32_16x16x128_f8f6f4 v[146:149], v[2:9], v[182:189], v[146:149], v197, v198 op_sel_hi:[0,0,0]
	v_mfma_scale_f32_16x16x128_f8f6f4 v[138:141], v[10:17], v[208:215], v[138:141], v197, v198 op_sel_hi:[0,0,0]
	v_mfma_scale_f32_16x16x128_f8f6f4 v[130:133], v[2:9], v[208:215], v[130:133], v197, v198 op_sel_hi:[0,0,0]
	v_mfma_scale_f32_16x16x128_f8f6f4 v[122:125], v[10:17], v[216:223], v[122:125], v197, v198 op_sel_hi:[0,0,0]
	v_mfma_scale_f32_16x16x128_f8f6f4 v[114:117], v[2:9], v[216:223], v[114:117], v197, v198 op_sel_hi:[0,0,0]
	v_mfma_scale_f32_16x16x128_f8f6f4 v[106:109], v[10:17], v[224:231], v[106:109], v197, v198 op_sel_hi:[0,0,0]
	v_mfma_scale_f32_16x16x128_f8f6f4 v[94:97], v[2:9], v[224:231], v[94:97], v197, v198 op_sel_hi:[0,0,0]
	s_setprio 0
	s_barrier
	s_mov_b32 m0, s41
	v_lshl_add_u64 v[182:183], s[20:21], 0, v[164:165]
	s_add_u32 s56, s20, 0x20000
	ds_read_b128 v[208:211], v196 offset:16384
	ds_read_b128 v[212:215], v196 offset:17408
	ds_read_b128 v[216:219], v196 offset:18432
	ds_read_b128 v[220:223], v196 offset:19456
	ds_read_b128 v[224:227], v196 offset:20480
	ds_read_b128 v[228:231], v196 offset:21504
	ds_read_b128 v[232:235], v196 offset:22528
	ds_read_b128 v[236:239], v196 offset:23552
	global_load_lds_dwordx4 v[182:183], off
	v_lshl_add_u64 v[184:185], s[20:21], 0, v[162:163]
	s_mov_b32 m0, s42
	s_addc_u32 s57, s21, 0
	global_load_lds_dwordx4 v[184:185], off
	v_lshl_add_u64 v[186:187], s[56:57], 0, v[164:165]
	s_mov_b32 m0, s43
	v_cndmask_b32_e32 v166, v206, v202, vcc
	global_load_lds_dwordx4 v[186:187], off
	v_lshl_add_u64 v[186:187], s[56:57], 0, v[162:163]
	s_mov_b32 m0, s44
	v_lshl_add_u64 v[188:189], s[22:23], 0, v[166:167]
	global_load_lds_dwordx4 v[186:187], off
	s_mov_b32 m0, s26
	v_cndmask_b32_e32 v186, v172, v203, vcc
	global_load_lds_dwordx4 v166, s[22:23]
	s_mov_b32 m0, s27
	v_mov_b32_e32 v187, v167
	global_load_lds_dwordx4 v186, s[22:23]
	s_waitcnt vmcnt(8)
	s_waitcnt lgkmcnt(0)
	v_lshl_add_u64 v[186:187], s[22:23], 0, v[186:187]
	s_barrier
	s_setprio 1
	s_nop 3
	s_waitcnt lgkmcnt(0)
	v_mfma_scale_f32_16x16x128_f8f6f4 v[82:85], v[26:33], v[208:215], v[82:85], v197, v198 op_sel_hi:[0,0,0]
	v_mfma_scale_f32_16x16x128_f8f6f4 v[70:73], v[18:25], v[208:215], v[70:73], v197, v198 op_sel_hi:[0,0,0]
	v_mfma_scale_f32_16x16x128_f8f6f4 v[78:81], v[26:33], v[216:223], v[78:81], v197, v198 op_sel_hi:[0,0,0]
	v_mfma_scale_f32_16x16x128_f8f6f4 v[66:69], v[18:25], v[216:223], v[66:69], v197, v198 op_sel_hi:[0,0,0]
	v_mfma_scale_f32_16x16x128_f8f6f4 v[58:61], v[26:33], v[224:231], v[58:61], v197, v198 op_sel_hi:[0,0,0]
	v_mfma_scale_f32_16x16x128_f8f6f4 v[50:53], v[18:25], v[224:231], v[50:53], v197, v198 op_sel_hi:[0,0,0]
	v_mfma_scale_f32_16x16x128_f8f6f4 v[42:45], v[26:33], v[232:239], v[42:45], v197, v198 op_sel_hi:[0,0,0]
	v_mfma_scale_f32_16x16x128_f8f6f4 v[34:37], v[18:25], v[232:239], v[34:37], v197, v198 op_sel_hi:[0,0,0]
	s_setprio 0
	s_setprio 1
	s_nop 3
	v_mfma_scale_f32_16x16x128_f8f6f4 v[102:105], v[10:17], v[208:215], v[102:105], v197, v198 op_sel_hi:[0,0,0]
	v_mfma_scale_f32_16x16x128_f8f6f4 v[90:93], v[2:9], v[208:215], v[90:93], v197, v198 op_sel_hi:[0,0,0]
	v_mfma_scale_f32_16x16x128_f8f6f4 v[86:89], v[10:17], v[216:223], v[86:89], v197, v198 op_sel_hi:[0,0,0]
	v_mfma_scale_f32_16x16x128_f8f6f4 v[74:77], v[2:9], v[216:223], v[74:77], v197, v198 op_sel_hi:[0,0,0]
	v_mfma_scale_f32_16x16x128_f8f6f4 v[62:65], v[10:17], v[224:231], v[62:65], v197, v198 op_sel_hi:[0,0,0]
	v_mfma_scale_f32_16x16x128_f8f6f4 v[54:57], v[2:9], v[224:231], v[54:57], v197, v198 op_sel_hi:[0,0,0]
	v_mfma_scale_f32_16x16x128_f8f6f4 v[46:49], v[10:17], v[232:239], v[46:49], v197, v198 op_sel_hi:[0,0,0]
	v_mfma_scale_f32_16x16x128_f8f6f4 v[38:41], v[2:9], v[232:239], v[38:41], v197, v198 op_sel_hi:[0,0,0]
	s_setprio 0
	s_barrier
; #define PG8_STAGE(bufoff, gbase, voff) do { _Pragma("unroll") for (int _i = 0; _i < 2; ++_i) \
;         __builtin_amdgcn_global_load_lds((const unsigned*)((const char*)(gbase) + (voff)[_i]), (PG8_LAS unsigned*)(lds + (bufoff) + ldsw + _i * 8192), 16, 0, 0); } while (0)
; #define PG8_STAGE_A(bufoff, gbase, h, nx) do { if constexpr (Sched::GATHER) { const unsigned vv_[2] = {(nx) ? vAn[h][0] : vA[h][0], (nx) ? vAn[h][1] : vA[h][1]}; PG8_STAGE(bufoff, gbase, vv_); } \
;         else { PG8_STAGE(bufoff, (gbase) + (h) * hstep, voffA); } } while (0)
; #define PG8_LDA(dst, b, h) do { _Pragma("unroll") for (int m = 0; m < 4; ++m) _Pragma("unroll") for (int k = 0; k < 2; ++k) dst[m][k] = *(const PG8_LAS bf16x8*)(lds + PG8_SA(b, h) + aoff + m * 2048 + k * 1024); } while (0)
; #define PG8_LDB(dst, b, h) do { _Pragma("unroll") for (int n = 0; n < 2; ++n) _Pragma("unroll") for (int k = 0; k < 2; ++k) dst[n][k] = *(const PG8_LAS bf16x8*)(lds + PG8_SB(b, h) + boff + n * 2048 + k * 1024); } while (0)
; #define PG8_WAIT_V(n) asm volatile("s_waitcnt vmcnt(" #n ")" ::: "memory")
; #define PG8_WAIT_L(n) asm volatile("s_waitcnt lgkmcnt(" #n ")" ::: "memory")
; #define PG8_BAR __builtin_amdgcn_s_barrier()
; #define PG8_SCHED __builtin_amdgcn_sched_barrier(0)
;     ...
;             PG8_LDB(B0, 1, 0); PG8_LDB(B1, 1, 1); PG8_SCHED; PG8_LDA(At, 1, 0); PG8_STAGE_A(PG8_SA(0, 1), a2, 1, last);
;             PG8_WAIT_V(8); PG8_WAIT_L(0); PG8_BAR; PG8_MMA(0, 0, At, B0); PG8_MMA(0, 1, At, B1); PG8_BAR; PG8_SCHED;
;             PG8_LDA(At, 1, 1); PG8_STAGE(PG8_SB(1, 0), b3, voffB); PG8_STAGE(PG8_SB(1, 1), b3 + hstepB, voffB); PG8_STAGE_A(PG8_SA(1, 0), a3, 0, last);
;             PG8_WAIT_V(8); PG8_WAIT_L(0); PG8_BAR; PG8_MMA(1, 0, At, B0); PG8_MMA(1, 1, At, B1); PG8_BAR; PG8_SCHED;
;     ...
;         if constexpr (F8) asm volatile("s_nop 15\n\ts_nop 15\n\ts_nop 15" ::: "memory");
	ds_read_b128 v[2:5], v199
	ds_read_b128 v[6:9], v199 offset:1024
	ds_read_b128 v[10:13], v199 offset:2048
	ds_read_b128 v[14:17], v199 offset:3072
	ds_read_b128 v[18:21], v200
	ds_read_b128 v[22:25], v200 offset:1024
	ds_read_b128 v[26:29], v200 offset:2048
	ds_read_b128 v[30:33], v200 offset:3072
	s_mov_b32 m0, s28
	v_cndmask_b32_e32 v166, v174, v204, vcc
	ds_read_b128 v[208:211], v196 offset:32768
	ds_read_b128 v[212:215], v196 offset:33792
	ds_read_b128 v[216:219], v196 offset:34816
	ds_read_b128 v[220:223], v196 offset:35840
	ds_read_b128 v[224:227], v196 offset:36864
	ds_read_b128 v[228:231], v196 offset:37888
	ds_read_b128 v[232:235], v196 offset:38912
	ds_read_b128 v[236:239], v196 offset:39936
	v_cndmask_b32_e32 v175, v176, v205, vcc
	global_load_lds_dwordx4 v166, s[22:23]
	s_mov_b32 m0, s29
	s_nop 0
	global_load_lds_dwordx4 v175, s[22:23]
	s_waitcnt vmcnt(8)
	s_waitcnt lgkmcnt(0)
	s_barrier
	s_setprio 1
	s_nop 3
	s_waitcnt lgkmcnt(0)
	v_mfma_scale_f32_16x16x128_f8f6f4 v[158:161], v[2:9], v[208:215], v[158:161], v197, v198 op_sel_hi:[0,0,0]
	v_mfma_scale_f32_16x16x128_f8f6f4 v[150:153], v[10:17], v[208:215], v[150:153], v197, v198 op_sel_hi:[0,0,0]
	v_mfma_scale_f32_16x16x128_f8f6f4 v[142:145], v[2:9], v[216:223], v[142:145], v197, v198 op_sel_hi:[0,0,0]
	v_mfma_scale_f32_16x16x128_f8f6f4 v[134:137], v[10:17], v[216:223], v[134:137], v197, v198 op_sel_hi:[0,0,0]
	v_mfma_scale_f32_16x16x128_f8f6f4 v[126:129], v[2:9], v[224:231], v[126:129], v197, v198 op_sel_hi:[0,0,0]
	v_mfma_scale_f32_16x16x128_f8f6f4 v[118:121], v[10:17], v[224:231], v[118:121], v197, v198 op_sel_hi:[0,0,0]
	v_mfma_scale_f32_16x16x128_f8f6f4 v[110:113], v[2:9], v[232:239], v[110:113], v197, v198 op_sel_hi:[0,0,0]
	v_mfma_scale_f32_16x16x128_f8f6f4 v[98:101], v[10:17], v[232:239], v[98:101], v197, v198 op_sel_hi:[0,0,0]
	s_setprio 0
	s_setprio 1
	s_nop 3
	v_mfma_scale_f32_16x16x128_f8f6f4 v[154:157], v[18:25], v[208:215], v[154:157], v197, v198 op_sel_hi:[0,0,0]
	v_mfma_scale_f32_16x16x128_f8f6f4 v[146:149], v[26:33], v[208:215], v[146:149], v197, v198 op_sel_hi:[0,0,0]
	v_mfma_scale_f32_16x16x128_f8f6f4 v[138:141], v[18:25], v[216:223], v[138:141], v197, v198 op_sel_hi:[0,0,0]
	v_mfma_scale_f32_16x16x128_f8f6f4 v[130:133], v[26:33], v[216:223], v[130:133], v197, v198 op_sel_hi:[0,0,0]
	v_mfma_scale_f32_16x16x128_f8f6f4 v[122:125], v[18:25], v[224:231], v[122:125], v197, v198 op_sel_hi:[0,0,0]
	v_mfma_scale_f32_16x16x128_f8f6f4 v[114:117], v[26:33], v[224:231], v[114:117], v197, v198 op_sel_hi:[0,0,0]
	v_mfma_scale_f32_16x16x128_f8f6f4 v[106:109], v[18:25], v[232:239], v[106:109], v197, v198 op_sel_hi:[0,0,0]
	v_mfma_scale_f32_16x16x128_f8f6f4 v[94:97], v[26:33], v[232:239], v[94:97], v197, v198 op_sel_hi:[0,0,0]
	s_setprio 0
	s_barrier
	s_mov_b32 m0, s45
	v_lshl_add_u64 v[182:183], v[182:183], 0, s[10:11]
	s_add_u32 s20, s20, 0x20080
	ds_read_b128 v[208:211], v196 offset:49152
	ds_read_b128 v[212:215], v196 offset:50176
	ds_read_b128 v[216:219], v196 offset:51200
	ds_read_b128 v[220:223], v196 offset:52224
	ds_read_b128 v[224:227], v196 offset:53248
	ds_read_b128 v[228:231], v196 offset:54272
	ds_read_b128 v[232:235], v196 offset:55296
	ds_read_b128 v[236:239], v196 offset:56320
	global_load_lds_dwordx4 v[182:183], off
	v_lshl_add_u64 v[182:183], v[184:185], 0, s[10:11]
	s_mov_b32 m0, s46
	s_addc_u32 s21, s21, 0
	global_load_lds_dwordx4 v[182:183], off
	v_lshl_add_u64 v[182:183], s[20:21], 0, v[164:165]
	s_mov_b32 m0, s47
	s_nop 0
	global_load_lds_dwordx4 v[182:183], off
	v_lshl_add_u64 v[182:183], s[20:21], 0, v[162:163]
	s_add_i32 m0, s47, 0x2000
	s_nop 0
	global_load_lds_dwordx4 v[182:183], off
	v_lshl_add_u64 v[182:183], v[188:189], 0, s[10:11]
	s_mov_b32 m0, s31
	s_nop 0
	global_load_lds_dwordx4 v[182:183], off
	v_lshl_add_u64 v[182:183], v[186:187], 0, s[10:11]
	s_mov_b32 m0, s34
	s_nop 0
	global_load_lds_dwordx4 v[182:183], off
	s_waitcnt vmcnt(8)
	s_waitcnt lgkmcnt(0)
	s_barrier
	s_setprio 1
	s_nop 3
	s_waitcnt lgkmcnt(0)
	v_mfma_scale_f32_16x16x128_f8f6f4 v[82:85], v[2:9], v[208:215], v[82:85], v197, v198 op_sel_hi:[0,0,0]
	v_mfma_scale_f32_16x16x128_f8f6f4 v[70:73], v[10:17], v[208:215], v[70:73], v197, v198 op_sel_hi:[0,0,0]
	v_mfma_scale_f32_16x16x128_f8f6f4 v[78:81], v[2:9], v[216:223], v[78:81], v197, v198 op_sel_hi:[0,0,0]
	v_mfma_scale_f32_16x16x128_f8f6f4 v[66:69], v[10:17], v[216:223], v[66:69], v197, v198 op_sel_hi:[0,0,0]
	v_mfma_scale_f32_16x16x128_f8f6f4 v[58:61], v[2:9], v[224:231], v[58:61], v197, v198 op_sel_hi:[0,0,0]
	v_mfma_scale_f32_16x16x128_f8f6f4 v[50:53], v[10:17], v[224:231], v[50:53], v197, v198 op_sel_hi:[0,0,0]
	v_mfma_scale_f32_16x16x128_f8f6f4 v[42:45], v[2:9], v[232:239], v[42:45], v197, v198 op_sel_hi:[0,0,0]
	v_mfma_scale_f32_16x16x128_f8f6f4 v[34:37], v[10:17], v[232:239], v[34:37], v197, v198 op_sel_hi:[0,0,0]
	s_setprio 0
	s_setprio 1
	s_nop 3
	v_mfma_scale_f32_16x16x128_f8f6f4 v[102:105], v[18:25], v[208:215], v[102:105], v197, v198 op_sel_hi:[0,0,0]
	v_mfma_scale_f32_16x16x128_f8f6f4 v[90:93], v[26:33], v[208:215], v[90:93], v197, v198 op_sel_hi:[0,0,0]
	v_mfma_scale_f32_16x16x128_f8f6f4 v[86:89], v[18:25], v[216:223], v[86:89], v197, v198 op_sel_hi:[0,0,0]
	v_mfma_scale_f32_16x16x128_f8f6f4 v[74:77], v[26:33], v[216:223], v[74:77], v197, v198 op_sel_hi:[0,0,0]
	v_mfma_scale_f32_16x16x128_f8f6f4 v[62:65], v[18:25], v[224:231], v[62:65], v197, v198 op_sel_hi:[0,0,0]
	v_mfma_scale_f32_16x16x128_f8f6f4 v[54:57], v[26:33], v[224:231], v[54:57], v197, v198 op_sel_hi:[0,0,0]
	v_mfma_scale_f32_16x16x128_f8f6f4 v[46:49], v[18:25], v[232:239], v[46:49], v197, v198 op_sel_hi:[0,0,0]
	v_mfma_scale_f32_16x16x128_f8f6f4 v[38:41], v[26:33], v[232:239], v[38:41], v197, v198 op_sel_hi:[0,0,0]
	s_setprio 0
	s_barrier
	s_add_i32 s54, s54, 2
	s_add_u32 s4, s4, 0x100
	s_addc_u32 s5, s5, 0
	s_cmp_gt_u32 s54, 5
	s_cbranch_scc0 .LBB0_1572
	s_and_b64 vcc, exec, s[14:15]
	s_cbranch_vccz .LBB0_1575
	s_barrier
